# early stash + in-epilogue alignment barrier also for P1 (EpiProj) and P6 (EpiDown)
# speedup vs baseline: 1.0191x; 1.0053x over previous
; #define PG8_STAGE(bufoff, base, uoff, voff) do { _Pragma("unroll") for (int _i = 0; _i < 2; ++_i) \
;         __builtin_amdgcn_raw_ptr_buffer_load_lds((base), (PG8_LAS void*)(lds + (bufoff) + ldsw + _i * 8192), 16, (int)(voff)[_i], (int)(uoff), 0, 0); } while (0)
; #define PG8_LDA(dst, b, h) do { _Pragma("unroll") for (int m = 0; m < 4; ++m) _Pragma("unroll") for (int k = 0; k < 2; ++k) dst[m][k] = *(const PG8_LAS bf16x8*)(lds + PG8_SA(b, h) + aoff + m * 2048 + k * 1024); } while (0)
; #define PG8_LDB(dst, b, h) do { _Pragma("unroll") for (int n = 0; n < 2; ++n) _Pragma("unroll") for (int k = 0; k < 2; ++k) dst[n][k] = *(const PG8_LAS bf16x8*)(lds + PG8_SB(b, h) + boff + n * 2048 + k * 1024); } while (0)
; #define PG8_WAIT_V(n) asm volatile("s_waitcnt vmcnt(" #n ")" ::: "memory")
; #define PG8_WAIT_L(n) asm volatile("s_waitcnt lgkmcnt(" #n ")" ::: "memory")
; #define PG8_BAR __builtin_amdgcn_s_barrier()
; #define PG8_SCHED __builtin_amdgcn_sched_barrier(0)
; template <class Epi, class Sched, bool GATHER, int MODE>
; __device__ __forceinline__ void gemm_phase(PG8_LAS unsigned char* lds, PG8_LAS unsigned* scr, const Gemm g, const Sched& S, const Epi& E, int tid_in) {
;     ...
;             const bool last = (t == nt - 2);
;             const int tt = __builtin_amdgcn_readfirstlane(t);
;             const unsigned a1 = cA + (unsigned)(tt + 1) * kstep;
;             const unsigned a2 = last ? nA : cA + (unsigned)(tt + 2) * kstep, b2 = last ? nB : cB + (unsigned)(tt + 2) * kstep;
;             const unsigned a3 = a2 + kstep, b3 = b2 + kstep;
;             unsigned s0[2], s1[2];
;             if (GATHER && last && has_next) { const u32x4 nx = gather_read(nxt); s0[0] = nx[0]; s0[1] = nx[1]; s1[0] = nx[2]; s1[1] = nx[3]; }
;             else { s0[0] = c0[0]; s0[1] = c0[1]; s1[0] = c1[0]; s1[1] = c1[1]; }
;             PG8_LDB(B0, 0, 0); PG8_LDB(B1, 0, 1); PG8_SCHED; PG8_LDA(At, 0, 0); PG8_STAGE(PG8_SA(1, 1), baseA, a1 + hstepA, c1);
;             PG8_WAIT_V(8); PG8_WAIT_L(0); PG8_BAR; PG8_MMA(0, 0, At, B0); PG8_MMA(0, 1, At, B1); PG8_BAR; PG8_SCHED;
;             PG8_LDA(At, 0, 1); PG8_STAGE(PG8_SB(0, 0), baseB, b2, voffB); PG8_STAGE(PG8_SB(0, 1), baseB, b2 + hstep, voffB); PG8_STAGE(PG8_SA(0, 0), baseA, a2, s0);
;             PG8_WAIT_V(8); PG8_WAIT_L(0); PG8_BAR; PG8_MMA(1, 0, At, B0); PG8_MMA(1, 1, At, B1); PG8_BAR; PG8_SCHED;
.LBB0_350:
	ds_read_b128 v[128:131], v184
	ds_read_b128 v[132:135], v184 offset:1024
	ds_read_b128 v[136:139], v184 offset:2048
	ds_read_b128 v[140:143], v184 offset:3072
	ds_read_b128 v[144:147], v185
	ds_read_b128 v[150:153], v185 offset:1024
	ds_read_b128 v[154:157], v185 offset:2048
	ds_read_b128 v[158:161], v185 offset:3072
	s_add_i32 s76, s77, 2
	s_lshl_b32 s80, s76, 7
	s_add_i32 s78, s80, 0x100
	s_add_i32 s79, s78, s72
	s_add_i32 s78, s78, s71
	s_cmp_eq_u32 s77, 4
	s_cselect_b32 s79, s74, s79
	s_cselect_b32 s78, s75, s78
	s_add_i32 s77, s79, 0x80
	s_add_i32 s80, s80, s73
	s_mov_b32 m0, s64
	ds_read_b128 v[204:207], v201
	ds_read_b128 v[208:211], v201 offset:1024
	ds_read_b128 v[212:215], v201 offset:2048
	ds_read_b128 v[216:219], v201 offset:3072
	ds_read_b128 v[220:223], v201 offset:4096
	ds_read_b128 v[224:227], v201 offset:5120
	ds_read_b128 v[228:231], v201 offset:6144
	ds_read_b128 v[232:235], v201 offset:7168
	buffer_load_dwordx4 v167, s[4:7], s80 offen lds
	s_mov_b32 m0, s65
	s_nop 0
	buffer_load_dwordx4 v180, s[4:7], s80 offen lds
	s_waitcnt vmcnt(8)
	s_waitcnt lgkmcnt(0)
	s_barrier
	s_setprio 1
	s_waitcnt lgkmcnt(7)
	v_mfma_i32_16x16x64_i8 v[120:123], v[128:131], v[204:207], v[120:123]
	s_waitcnt lgkmcnt(6)
	v_mfma_i32_16x16x64_i8 v[120:123], v[132:135], v[208:211], v[120:123]
	v_mfma_i32_16x16x64_i8 v[112:115], v[136:139], v[204:207], v[112:115]
	s_nop 0
	v_mfma_i32_16x16x64_i8 v[112:115], v[140:143], v[208:211], v[112:115]
	s_waitcnt lgkmcnt(5)
	v_mfma_i32_16x16x64_i8 v[108:111], v[128:131], v[212:215], v[108:111]
	s_waitcnt lgkmcnt(4)
	v_mfma_i32_16x16x64_i8 v[108:111], v[132:135], v[216:219], v[108:111]
	v_mfma_i32_16x16x64_i8 v[88:91], v[136:139], v[212:215], v[88:91]
	s_nop 0
	v_mfma_i32_16x16x64_i8 v[88:91], v[140:143], v[216:219], v[88:91]
	s_waitcnt lgkmcnt(3)
	v_mfma_i32_16x16x64_i8 v[60:63], v[128:131], v[220:223], v[60:63]
	s_waitcnt lgkmcnt(2)
	v_mfma_i32_16x16x64_i8 v[60:63], v[132:135], v[224:227], v[60:63]
	v_mfma_i32_16x16x64_i8 v[56:59], v[136:139], v[220:223], v[56:59]
	s_nop 0
	v_mfma_i32_16x16x64_i8 v[56:59], v[140:143], v[224:227], v[56:59]
	s_waitcnt lgkmcnt(1)
	v_mfma_i32_16x16x64_i8 v[28:31], v[128:131], v[228:231], v[28:31]
	s_waitcnt lgkmcnt(0)
	v_mfma_i32_16x16x64_i8 v[28:31], v[132:135], v[232:235], v[28:31]
	v_mfma_i32_16x16x64_i8 v[24:27], v[136:139], v[228:231], v[24:27]
	s_nop 0
	v_mfma_i32_16x16x64_i8 v[24:27], v[140:143], v[232:235], v[24:27]
	s_setprio 0
	s_setprio 1
	v_mfma_i32_16x16x64_i8 v[124:127], v[144:147], v[204:207], v[124:127]
	s_nop 0
	v_mfma_i32_16x16x64_i8 v[124:127], v[150:153], v[208:211], v[124:127]
	v_mfma_i32_16x16x64_i8 v[116:119], v[154:157], v[204:207], v[116:119]
	s_nop 0
	v_mfma_i32_16x16x64_i8 v[116:119], v[158:161], v[208:211], v[116:119]
	v_mfma_i32_16x16x64_i8 v[104:107], v[144:147], v[212:215], v[104:107]
	s_nop 0
	v_mfma_i32_16x16x64_i8 v[104:107], v[150:153], v[216:219], v[104:107]
	v_mfma_i32_16x16x64_i8 v[100:103], v[154:157], v[212:215], v[100:103]
	s_nop 0
	v_mfma_i32_16x16x64_i8 v[100:103], v[158:161], v[216:219], v[100:103]
	v_mfma_i32_16x16x64_i8 v[76:79], v[144:147], v[220:223], v[76:79]
	s_nop 0
	v_mfma_i32_16x16x64_i8 v[76:79], v[150:153], v[224:227], v[76:79]
	v_mfma_i32_16x16x64_i8 v[68:71], v[154:157], v[220:223], v[68:71]
	s_nop 0
	v_mfma_i32_16x16x64_i8 v[68:71], v[158:161], v[224:227], v[68:71]
	v_mfma_i32_16x16x64_i8 v[44:47], v[144:147], v[228:231], v[44:47]
	s_nop 0
	v_mfma_i32_16x16x64_i8 v[44:47], v[150:153], v[232:235], v[44:47]
	v_mfma_i32_16x16x64_i8 v[32:35], v[154:157], v[228:231], v[32:35]
	s_nop 0
	v_mfma_i32_16x16x64_i8 v[32:35], v[158:161], v[232:235], v[32:35]
	s_setprio 0
	s_barrier
	s_mov_b32 m0, s51
	ds_read_b128 v[204:207], v201 offset:16384
	ds_read_b128 v[208:211], v201 offset:17408
	ds_read_b128 v[212:215], v201 offset:18432
	ds_read_b128 v[216:219], v201 offset:19456
	ds_read_b128 v[220:223], v201 offset:20480
	ds_read_b128 v[224:227], v201 offset:21504
	ds_read_b128 v[228:231], v201 offset:22528
	ds_read_b128 v[232:235], v201 offset:23552
	buffer_load_dwordx4 v168, s[40:43], s78 offen lds
	s_mov_b32 m0, s52
	s_add_i32 s80, s78, 0x20000
	buffer_load_dwordx4 v181, s[40:43], s78 offen lds
	s_mov_b32 m0, s53
	s_nop 0
	buffer_load_dwordx4 v168, s[40:43], s80 offen lds
	s_mov_b32 m0, s54
	s_nop 0
	buffer_load_dwordx4 v181, s[40:43], s80 offen lds
	s_mov_b32 m0, s50
	s_nop 0
	buffer_load_dwordx4 v167, s[4:7], s79 offen lds
	s_mov_b32 m0, s55
	s_nop 0
	buffer_load_dwordx4 v180, s[4:7], s79 offen lds
	s_waitcnt vmcnt(8)
	s_waitcnt lgkmcnt(0)
	s_barrier
; #define PG8_STAGE(bufoff, base, uoff, voff) do { _Pragma("unroll") for (int _i = 0; _i < 2; ++_i) \
;         __builtin_amdgcn_raw_ptr_buffer_load_lds((base), (PG8_LAS void*)(lds + (bufoff) + ldsw + _i * 8192), 16, (int)(voff)[_i], (int)(uoff), 0, 0); } while (0)
; #define PG8_LDA(dst, b, h) do { _Pragma("unroll") for (int m = 0; m < 4; ++m) _Pragma("unroll") for (int k = 0; k < 2; ++k) dst[m][k] = *(const PG8_LAS bf16x8*)(lds + PG8_SA(b, h) + aoff + m * 2048 + k * 1024); } while (0)
; #define PG8_LDB(dst, b, h) do { _Pragma("unroll") for (int n = 0; n < 2; ++n) _Pragma("unroll") for (int k = 0; k < 2; ++k) dst[n][k] = *(const PG8_LAS bf16x8*)(lds + PG8_SB(b, h) + boff + n * 2048 + k * 1024); } while (0)
; #define PG8_WAIT_V(n) asm volatile("s_waitcnt vmcnt(" #n ")" ::: "memory")
; #define PG8_WAIT_L(n) asm volatile("s_waitcnt lgkmcnt(" #n ")" ::: "memory")
; #define PG8_BAR __builtin_amdgcn_s_barrier()
; #define PG8_SCHED __builtin_amdgcn_sched_barrier(0)
; template <class Epi, class Sched, bool GATHER, int MODE>
; __device__ __forceinline__ void gemm_phase(PG8_LAS unsigned char* lds, PG8_LAS unsigned* scr, const Gemm g, const Sched& S, const Epi& E, int tid_in) {
;     ...
;             PG8_WAIT_V(8); PG8_WAIT_L(0); PG8_BAR; PG8_MMA(1, 0, At, B0); PG8_MMA(1, 1, At, B1); PG8_BAR; PG8_SCHED;
;             PG8_LDB(B0, 1, 0); PG8_LDB(B1, 1, 1); PG8_SCHED; PG8_LDA(At, 1, 0); PG8_STAGE(PG8_SA(0, 1), baseA, a2 + hstepA, s1);
;             PG8_WAIT_V(8); PG8_WAIT_L(0); PG8_BAR; PG8_MMA(0, 0, At, B0); PG8_MMA(0, 1, At, B1); PG8_BAR; PG8_SCHED;
	s_setprio 1
	s_waitcnt lgkmcnt(7)
	v_mfma_i32_16x16x64_i8 v[84:87], v[128:131], v[204:207], v[84:87]
	s_waitcnt lgkmcnt(6)
	v_mfma_i32_16x16x64_i8 v[84:87], v[132:135], v[208:211], v[84:87]
	v_mfma_i32_16x16x64_i8 v[80:83], v[136:139], v[204:207], v[80:83]
	s_nop 0
	v_mfma_i32_16x16x64_i8 v[80:83], v[140:143], v[208:211], v[80:83]
	s_waitcnt lgkmcnt(5)
	v_mfma_i32_16x16x64_i8 v[52:55], v[128:131], v[212:215], v[52:55]
	s_waitcnt lgkmcnt(4)
	v_mfma_i32_16x16x64_i8 v[52:55], v[132:135], v[216:219], v[52:55]
	v_mfma_i32_16x16x64_i8 v[48:51], v[136:139], v[212:215], v[48:51]
	s_nop 0
	v_mfma_i32_16x16x64_i8 v[48:51], v[140:143], v[216:219], v[48:51]
	s_waitcnt lgkmcnt(3)
	v_mfma_i32_16x16x64_i8 v[20:23], v[128:131], v[220:223], v[20:23]
	s_waitcnt lgkmcnt(2)
	v_mfma_i32_16x16x64_i8 v[20:23], v[132:135], v[224:227], v[20:23]
	v_mfma_i32_16x16x64_i8 v[16:19], v[136:139], v[220:223], v[16:19]
	s_nop 0
	v_mfma_i32_16x16x64_i8 v[16:19], v[140:143], v[224:227], v[16:19]
	s_waitcnt lgkmcnt(1)
	v_mfma_i32_16x16x64_i8 v[8:11], v[128:131], v[228:231], v[8:11]
	s_waitcnt lgkmcnt(0)
	v_mfma_i32_16x16x64_i8 v[8:11], v[132:135], v[232:235], v[8:11]
	v_mfma_i32_16x16x64_i8 v[0:3], v[136:139], v[228:231], v[0:3]
	s_nop 0
	v_mfma_i32_16x16x64_i8 v[0:3], v[140:143], v[232:235], v[0:3]
	s_setprio 0
	s_setprio 1
	v_mfma_i32_16x16x64_i8 v[96:99], v[144:147], v[204:207], v[96:99]
	s_nop 0
	v_mfma_i32_16x16x64_i8 v[96:99], v[150:153], v[208:211], v[96:99]
	v_mfma_i32_16x16x64_i8 v[92:95], v[154:157], v[204:207], v[92:95]
	s_nop 0
	v_mfma_i32_16x16x64_i8 v[92:95], v[158:161], v[208:211], v[92:95]
	v_mfma_i32_16x16x64_i8 v[72:75], v[144:147], v[212:215], v[72:75]
	s_nop 0
	v_mfma_i32_16x16x64_i8 v[72:75], v[150:153], v[216:219], v[72:75]
	v_mfma_i32_16x16x64_i8 v[64:67], v[154:157], v[212:215], v[64:67]
	s_nop 0
	v_mfma_i32_16x16x64_i8 v[64:67], v[158:161], v[216:219], v[64:67]
	v_mfma_i32_16x16x64_i8 v[40:43], v[144:147], v[220:223], v[40:43]
	s_nop 0
	v_mfma_i32_16x16x64_i8 v[40:43], v[150:153], v[224:227], v[40:43]
	v_mfma_i32_16x16x64_i8 v[36:39], v[154:157], v[220:223], v[36:39]
	s_nop 0
	v_mfma_i32_16x16x64_i8 v[36:39], v[158:161], v[224:227], v[36:39]
	v_mfma_i32_16x16x64_i8 v[12:15], v[144:147], v[228:231], v[12:15]
	s_nop 0
	v_mfma_i32_16x16x64_i8 v[12:15], v[150:153], v[232:235], v[12:15]
	v_mfma_i32_16x16x64_i8 v[4:7], v[154:157], v[228:231], v[4:7]
	s_nop 0
	v_mfma_i32_16x16x64_i8 v[4:7], v[158:161], v[232:235], v[4:7]
	s_setprio 0
	s_barrier
	ds_read_b128 v[128:131], v148
	ds_read_b128 v[132:135], v148 offset:1024
	ds_read_b128 v[136:139], v148 offset:2048
	ds_read_b128 v[140:143], v148 offset:3072
	ds_read_b128 v[144:147], v149
	ds_read_b128 v[150:153], v149 offset:1024
	ds_read_b128 v[154:157], v149 offset:2048
	ds_read_b128 v[158:161], v149 offset:3072
	s_add_i32 s79, s79, 0x20000
	s_mov_b32 m0, s56
	ds_read_b128 v[204:207], v201 offset:32768
	ds_read_b128 v[208:211], v201 offset:33792
	ds_read_b128 v[212:215], v201 offset:34816
	ds_read_b128 v[216:219], v201 offset:35840
	ds_read_b128 v[220:223], v201 offset:36864
	ds_read_b128 v[224:227], v201 offset:37888
	ds_read_b128 v[228:231], v201 offset:38912
	ds_read_b128 v[232:235], v201 offset:39936
	buffer_load_dwordx4 v167, s[4:7], s79 offen lds
	s_mov_b32 m0, s57
	s_nop 0
	buffer_load_dwordx4 v180, s[4:7], s79 offen lds
	s_waitcnt vmcnt(8)
	s_waitcnt lgkmcnt(0)
	s_barrier
	s_setprio 1
	s_waitcnt lgkmcnt(7)
	v_mfma_i32_16x16x64_i8 v[120:123], v[128:131], v[204:207], v[120:123]
	s_waitcnt lgkmcnt(6)
	v_mfma_i32_16x16x64_i8 v[120:123], v[132:135], v[208:211], v[120:123]
	v_mfma_i32_16x16x64_i8 v[112:115], v[136:139], v[204:207], v[112:115]
	s_nop 0
	v_mfma_i32_16x16x64_i8 v[112:115], v[140:143], v[208:211], v[112:115]
	s_waitcnt lgkmcnt(5)
	v_mfma_i32_16x16x64_i8 v[108:111], v[128:131], v[212:215], v[108:111]
	s_waitcnt lgkmcnt(4)
	v_mfma_i32_16x16x64_i8 v[108:111], v[132:135], v[216:219], v[108:111]
	v_mfma_i32_16x16x64_i8 v[88:91], v[136:139], v[212:215], v[88:91]
	s_nop 0
	v_mfma_i32_16x16x64_i8 v[88:91], v[140:143], v[216:219], v[88:91]
	s_waitcnt lgkmcnt(3)
	v_mfma_i32_16x16x64_i8 v[60:63], v[128:131], v[220:223], v[60:63]
	s_waitcnt lgkmcnt(2)
	v_mfma_i32_16x16x64_i8 v[60:63], v[132:135], v[224:227], v[60:63]
	v_mfma_i32_16x16x64_i8 v[56:59], v[136:139], v[220:223], v[56:59]
	s_nop 0
	v_mfma_i32_16x16x64_i8 v[56:59], v[140:143], v[224:227], v[56:59]
	s_waitcnt lgkmcnt(1)
	v_mfma_i32_16x16x64_i8 v[28:31], v[128:131], v[228:231], v[28:31]
	s_waitcnt lgkmcnt(0)
	v_mfma_i32_16x16x64_i8 v[28:31], v[132:135], v[232:235], v[28:31]
	v_mfma_i32_16x16x64_i8 v[24:27], v[136:139], v[228:231], v[24:27]
	s_nop 0
	v_mfma_i32_16x16x64_i8 v[24:27], v[140:143], v[232:235], v[24:27]
	s_setprio 0
	s_setprio 1
	v_mfma_i32_16x16x64_i8 v[124:127], v[144:147], v[204:207], v[124:127]
	s_nop 0
	v_mfma_i32_16x16x64_i8 v[124:127], v[150:153], v[208:211], v[124:127]
	v_mfma_i32_16x16x64_i8 v[116:119], v[154:157], v[204:207], v[116:119]
	s_nop 0
	v_mfma_i32_16x16x64_i8 v[116:119], v[158:161], v[208:211], v[116:119]
	v_mfma_i32_16x16x64_i8 v[104:107], v[144:147], v[212:215], v[104:107]
	s_nop 0
	v_mfma_i32_16x16x64_i8 v[104:107], v[150:153], v[216:219], v[104:107]
	v_mfma_i32_16x16x64_i8 v[100:103], v[154:157], v[212:215], v[100:103]
	s_nop 0
	v_mfma_i32_16x16x64_i8 v[100:103], v[158:161], v[216:219], v[100:103]
	v_mfma_i32_16x16x64_i8 v[76:79], v[144:147], v[220:223], v[76:79]
	s_nop 0
	v_mfma_i32_16x16x64_i8 v[76:79], v[150:153], v[224:227], v[76:79]
	v_mfma_i32_16x16x64_i8 v[68:71], v[154:157], v[220:223], v[68:71]
	s_nop 0
	v_mfma_i32_16x16x64_i8 v[68:71], v[158:161], v[224:227], v[68:71]
	v_mfma_i32_16x16x64_i8 v[44:47], v[144:147], v[228:231], v[44:47]
	s_nop 0
	v_mfma_i32_16x16x64_i8 v[44:47], v[150:153], v[232:235], v[44:47]
	v_mfma_i32_16x16x64_i8 v[32:35], v[154:157], v[228:231], v[32:35]
	s_nop 0
	v_mfma_i32_16x16x64_i8 v[32:35], v[158:161], v[232:235], v[32:35]
	s_setprio 0
	s_barrier
	s_cmp_eq_u32 s76, 6
	s_cbranch_scc0 .Lp1_nostash
	ds_write_b32 v182, v202
; #define PG8_LAS __attribute__((address_space(3)))
;     __device__ __forceinline__ void stash(const Pre2& p, PG8_LAS unsigned* scr, int t) const { scr[t] = p.a; if (t < 256) scr[512 + t] = p.b; }
; #define PG8_STAGE(bufoff, base, uoff, voff) do { _Pragma("unroll") for (int _i = 0; _i < 2; ++_i) \
;         __builtin_amdgcn_raw_ptr_buffer_load_lds((base), (PG8_LAS void*)(lds + (bufoff) + ldsw + _i * 8192), 16, (int)(voff)[_i], (int)(uoff), 0, 0); } while (0)
; #define PG8_LDA(dst, b, h) do { _Pragma("unroll") for (int m = 0; m < 4; ++m) _Pragma("unroll") for (int k = 0; k < 2; ++k) dst[m][k] = *(const PG8_LAS bf16x8*)(lds + PG8_SA(b, h) + aoff + m * 2048 + k * 1024); } while (0)
; #define PG8_WAIT_V(n) asm volatile("s_waitcnt vmcnt(" #n ")" ::: "memory")
; #define PG8_WAIT_L(n) asm volatile("s_waitcnt lgkmcnt(" #n ")" ::: "memory")
; #define PG8_BAR __builtin_amdgcn_s_barrier()
; #define PG8_SCHED __builtin_amdgcn_sched_barrier(0)
;     __device__ __forceinline__ void operator()(const i32x4 (&acc)[2][2][4][2], const Unit& u, int wr, int wc, int fr, int fq, PG8_LAS unsigned* scr) const {
;         const int row0 = u.pm * BM + wr * 64 + fr, col0 = u.pn * BM + wc * 32 + 8 * fq;
;         f32x4 cs[2][2];
; #pragma unroll
;         for (int bj = 0; bj < 2; ++bj)
; #pragma unroll
;             for (int n = 0; n < 2; ++n) cs[bj][n] = *(const PG8_LAS f32x4*)(scr + 256 + bj * HALF + wc * 32 + 8 * fq + 4 * n) * (1.0f / 127.0f);
; #pragma unroll
;         for (int ai = 0; ai < 2; ++ai)
; #pragma unroll
;             for (int m = 0; m < 4; ++m) { const int r = ai * HALF + wr * 64 + m * 16 + fr; const float rs = __uint_as_float(scr[r]); bf16_t* rowp = O + (size_t)(u.pm * BM + r) * ldc + col0;
; template <class Epi, class Sched, bool GATHER, int MODE>
; __device__ __forceinline__ void gemm_phase(PG8_LAS unsigned char* lds, PG8_LAS unsigned* scr, const Gemm g, const Sched& S, const Epi& E, int tid_in) {
;     ...
;             PG8_LDA(At, 1, 1); PG8_STAGE(PG8_SB(1, 0), baseB, b3, voffB); PG8_STAGE(PG8_SB(1, 1), baseB, b3 + hstep, voffB); PG8_STAGE(PG8_SA(1, 0), baseA, a3, s0);
;             PG8_WAIT_V(8); PG8_WAIT_L(0); PG8_BAR; PG8_MMA(1, 0, At, B0); PG8_MMA(1, 1, At, B1); PG8_BAR; PG8_SCHED;
;         }
;         asm volatile("s_nop 15\n\ts_nop 7" ::: "memory");
;         if (wr == 0) PG8_BAR;
;         if (Epi::HAS_PRE) { E.stash(pre, scr, tid); PG8_WAIT_L(0); PG8_BAR; }
.Lp1_nostash:
	s_mov_b32 m0, s58
	s_add_i32 s79, s78, 0x80
	ds_read_b128 v[204:207], v201 offset:49152
	ds_read_b128 v[208:211], v201 offset:50176
	ds_read_b128 v[212:215], v201 offset:51200
	ds_read_b128 v[216:219], v201 offset:52224
	ds_read_b128 v[220:223], v201 offset:53248
	ds_read_b128 v[224:227], v201 offset:54272
	ds_read_b128 v[228:231], v201 offset:55296
	ds_read_b128 v[232:235], v201 offset:56320
	buffer_load_dwordx4 v168, s[40:43], s79 offen lds
	s_mov_b32 m0, s59
	s_add_i32 s78, s78, 0x20080
	buffer_load_dwordx4 v181, s[40:43], s79 offen lds
	s_mov_b32 m0, s62
	s_nop 0
	buffer_load_dwordx4 v168, s[40:43], s78 offen lds
	s_mov_b32 m0, s63
	s_nop 0
	buffer_load_dwordx4 v181, s[40:43], s78 offen lds
	s_mov_b32 m0, s60
	s_nop 0
	buffer_load_dwordx4 v167, s[4:7], s77 offen lds
	s_mov_b32 m0, s61
	s_nop 0
	buffer_load_dwordx4 v180, s[4:7], s77 offen lds
	s_waitcnt vmcnt(8)
	s_waitcnt lgkmcnt(0)
	s_barrier
	s_setprio 1
	s_waitcnt lgkmcnt(7)
	v_mfma_i32_16x16x64_i8 v[84:87], v[128:131], v[204:207], v[84:87]
	s_waitcnt lgkmcnt(6)
	v_mfma_i32_16x16x64_i8 v[84:87], v[132:135], v[208:211], v[84:87]
	v_mfma_i32_16x16x64_i8 v[80:83], v[136:139], v[204:207], v[80:83]
	s_nop 0
	v_mfma_i32_16x16x64_i8 v[80:83], v[140:143], v[208:211], v[80:83]
	s_waitcnt lgkmcnt(5)
	v_mfma_i32_16x16x64_i8 v[52:55], v[128:131], v[212:215], v[52:55]
	s_waitcnt lgkmcnt(4)
	v_mfma_i32_16x16x64_i8 v[52:55], v[132:135], v[216:219], v[52:55]
	v_mfma_i32_16x16x64_i8 v[48:51], v[136:139], v[212:215], v[48:51]
	s_nop 0
	v_mfma_i32_16x16x64_i8 v[48:51], v[140:143], v[216:219], v[48:51]
	s_waitcnt lgkmcnt(3)
	v_mfma_i32_16x16x64_i8 v[20:23], v[128:131], v[220:223], v[20:23]
	s_waitcnt lgkmcnt(2)
	v_mfma_i32_16x16x64_i8 v[20:23], v[132:135], v[224:227], v[20:23]
	v_mfma_i32_16x16x64_i8 v[16:19], v[136:139], v[220:223], v[16:19]
	s_nop 0
	v_mfma_i32_16x16x64_i8 v[16:19], v[140:143], v[224:227], v[16:19]
	s_waitcnt lgkmcnt(1)
	v_mfma_i32_16x16x64_i8 v[8:11], v[128:131], v[228:231], v[8:11]
	s_waitcnt lgkmcnt(0)
	v_mfma_i32_16x16x64_i8 v[8:11], v[132:135], v[232:235], v[8:11]
	v_mfma_i32_16x16x64_i8 v[0:3], v[136:139], v[228:231], v[0:3]
	s_nop 0
	v_mfma_i32_16x16x64_i8 v[0:3], v[140:143], v[232:235], v[0:3]
	s_setprio 0
	s_setprio 1
	v_mfma_i32_16x16x64_i8 v[96:99], v[144:147], v[204:207], v[96:99]
	s_nop 0
	v_mfma_i32_16x16x64_i8 v[96:99], v[150:153], v[208:211], v[96:99]
	v_mfma_i32_16x16x64_i8 v[92:95], v[154:157], v[204:207], v[92:95]
	s_nop 0
	v_mfma_i32_16x16x64_i8 v[92:95], v[158:161], v[208:211], v[92:95]
	v_mfma_i32_16x16x64_i8 v[72:75], v[144:147], v[212:215], v[72:75]
	s_nop 0
	v_mfma_i32_16x16x64_i8 v[72:75], v[150:153], v[216:219], v[72:75]
	v_mfma_i32_16x16x64_i8 v[64:67], v[154:157], v[212:215], v[64:67]
	s_nop 0
	v_mfma_i32_16x16x64_i8 v[64:67], v[158:161], v[216:219], v[64:67]
	v_mfma_i32_16x16x64_i8 v[40:43], v[144:147], v[220:223], v[40:43]
	s_nop 0
	v_mfma_i32_16x16x64_i8 v[40:43], v[150:153], v[224:227], v[40:43]
	v_mfma_i32_16x16x64_i8 v[36:39], v[154:157], v[220:223], v[36:39]
	s_nop 0
	v_mfma_i32_16x16x64_i8 v[36:39], v[158:161], v[224:227], v[36:39]
	v_mfma_i32_16x16x64_i8 v[12:15], v[144:147], v[228:231], v[12:15]
	s_nop 0
	v_mfma_i32_16x16x64_i8 v[12:15], v[150:153], v[232:235], v[12:15]
	v_mfma_i32_16x16x64_i8 v[4:7], v[154:157], v[228:231], v[4:7]
	s_nop 0
	v_mfma_i32_16x16x64_i8 v[4:7], v[158:161], v[232:235], v[4:7]
	s_setprio 0
	s_barrier
	s_cmp_gt_u32 s76, 5
	s_mov_b32 s77, s76
	s_cbranch_scc0 .LBB0_350
	s_nop 15
	s_nop 7
.LBB0_353:
	v_mov_b32_e32 v132, v164
	s_mov_b32 s42, 0x3c010204
	v_lshrrev_b32_e32 v128, 1, v132
	v_and_b32_e32 v152, 0x60, v128
	v_and_b32_e32 v153, 24, v128
	v_lshlrev_b32_e32 v128, 2, v152
	v_lshlrev_b32_e32 v129, 2, v153
	v_add3_u32 v138, s82, v128, v129
	ds_read_b128 v[128:131], v138
	v_and_b32_e32 v154, 15, v132
	v_ashrrev_i32_e32 v155, 2, v132
	ds_read_b128 v[132:135], v138 offset:16
	ds_read_b128 v[144:147], v138 offset:512
	ds_read_b128 v[148:151], v138 offset:528
	s_waitcnt lgkmcnt(3)
	v_pk_mul_f32 v[136:137], v[130:131], s[42:43] op_sel_hi:[1,0]
	v_pk_mul_f32 v[142:143], v[128:129], s[42:43] op_sel_hi:[1,0]
	s_waitcnt lgkmcnt(2)
	v_pk_mul_f32 v[138:139], v[134:135], s[42:43] op_sel_hi:[1,0]
	v_pk_mul_f32 v[140:141], v[132:133], s[42:43] op_sel_hi:[1,0]
	s_waitcnt lgkmcnt(1)
	v_pk_mul_f32 v[132:133], v[146:147], s[42:43] op_sel_hi:[1,0]
	v_pk_mul_f32 v[134:135], v[144:145], s[42:43] op_sel_hi:[1,0]
	s_waitcnt lgkmcnt(0)
	v_pk_mul_f32 v[128:129], v[150:151], s[42:43] op_sel_hi:[1,0]
	v_pk_mul_f32 v[130:131], v[148:149], s[42:43] op_sel_hi:[1,0]
	s_lshl_b32 s42, s70, 8
	v_or3_b32 v146, v152, s42, v153
	s_movk_i32 s42, 0xffc0
	v_and_or_b32 v158, v155, s42, v154
	v_lshl_add_u32 v151, v158, 2, s88
	ds_read2st64_b32 v[148:149], v151 offset1:2
	v_cvt_f32_i32_e32 v121, v121
	v_cvt_f32_i32_e32 v123, v123
	v_cvt_f32_i32_e32 v122, v122
	v_cvt_f32_i32_e32 v120, v120
	v_cvt_f32_i32_e32 v113, v113
	v_cvt_f32_i32_e32 v115, v115
	v_cvt_f32_i32_e32 v114, v114
	v_cvt_f32_i32_e32 v112, v112
	s_lshl_b32 s42, s69, 8
	s_waitcnt lgkmcnt(0)
; #define GAS __attribute__((address_space(1)))
; #define PG8_LAS __attribute__((address_space(3)))
; __device__ __forceinline__ unsigned cvt_pk_bf16(float lo, float hi) { const f32x2c v = {lo, hi}; const bf16x2c b = __builtin_convertvector(v, bf16x2c); return __builtin_bit_cast(unsigned, b); }
;     __device__ __forceinline__ void operator()(const i32x4 (&acc)[2][2][4][2], const Unit& u, int wr, int wc, int fr, int fq, PG8_LAS unsigned* scr) const {
;     ...
;             for (int n = 0; n < 2; ++n) cs[bj][n] = *(const PG8_LAS f32x4*)(scr + 256 + bj * HALF + wc * 32 + 8 * fq + 4 * n) * (1.0f / 127.0f);
; #pragma unroll
;         for (int ai = 0; ai < 2; ++ai)
; #pragma unroll
;             for (int m = 0; m < 4; ++m) { const int r = ai * HALF + wr * 64 + m * 16 + fr; const float rs = __uint_as_float(scr[r]); bf16_t* rowp = O + (size_t)(u.pm * BM + r) * ldc + col0;
; #pragma unroll
;                 for (int bj = 0; bj < 2; ++bj) { const f32x4 v0 = __builtin_convertvector(acc[ai][bj][m][0], f32x4) * (cs[bj][0] * rs), v1 = __builtin_convertvector(acc[ai][bj][m][1], f32x4) * (cs[bj][1] * rs);
;                     u32x4 w; w.x = cvt_pk_bf16(v0[0], v0[1]); w.y = cvt_pk_bf16(v0[2], v0[3]); w.z = cvt_pk_bf16(v1[0], v1[1]); w.w = cvt_pk_bf16(v1[2], v1[3]);
;                     *(GAS u32x4*)(rowp + bj * HALF) = w; } }
	v_pk_mul_f32 v[154:155], v[136:137], v[148:149] op_sel_hi:[1,0]
	v_pk_mul_f32 v[156:157], v[142:143], v[148:149] op_sel_hi:[1,0]
	v_ashrrev_i32_e32 v147, 31, v146
	v_add_u32_e32 v150, s42, v158
	v_mov_b64_e32 v[144:145], s[22:23]
	v_pk_mul_f32 v[122:123], v[154:155], v[122:123]
	v_pk_mul_f32 v[120:121], v[156:157], v[120:121]
	v_pk_mul_f32 v[154:155], v[138:139], v[148:149] op_sel_hi:[1,0]
	v_pk_mul_f32 v[156:157], v[140:141], v[148:149] op_sel_hi:[1,0]
	v_mad_i64_i32 v[152:153], s[70:71], v150, s33, v[144:145]
	v_lshlrev_b64 v[146:147], 1, v[146:147]
	v_pk_mul_f32 v[154:155], v[154:155], v[114:115]
	v_pk_mul_f32 v[114:115], v[156:157], v[112:113]
	v_lshl_add_u64 v[152:153], v[152:153], 0, v[146:147]
	v_cvt_pk_bf16_f32 v112, v120, v121
	v_cvt_pk_bf16_f32 v113, v122, v123
	v_cvt_pk_bf16_f32 v114, v114, v115
	v_cvt_pk_bf16_f32 v115, v154, v155
	global_store_dwordx4 v[152:153], v[112:115], off
	v_cvt_f32_i32_e32 v117, v117
	v_cvt_f32_i32_e32 v119, v119
	v_cvt_f32_i32_e32 v113, v125
	v_cvt_f32_i32_e32 v115, v127
	v_cvt_f32_i32_e32 v114, v126
	v_cvt_f32_i32_e32 v112, v124
	v_cvt_f32_i32_e32 v118, v118
	v_cvt_f32_i32_e32 v116, v116
	v_pk_mul_f32 v[120:121], v[132:133], v[148:149] op_sel_hi:[1,0]
	v_pk_mul_f32 v[122:123], v[134:135], v[148:149] op_sel_hi:[1,0]
	v_pk_mul_f32 v[114:115], v[120:121], v[114:115]
	v_pk_mul_f32 v[112:113], v[122:123], v[112:113]
	v_pk_mul_f32 v[120:121], v[128:129], v[148:149] op_sel_hi:[1,0]
	v_pk_mul_f32 v[122:123], v[130:131], v[148:149] op_sel_hi:[1,0]
	v_pk_mul_f32 v[118:119], v[120:121], v[118:119]
	v_pk_mul_f32 v[116:117], v[122:123], v[116:117]
	v_cvt_pk_bf16_f32 v112, v112, v113
	v_cvt_pk_bf16_f32 v113, v114, v115
	v_cvt_pk_bf16_f32 v114, v116, v117
	v_cvt_pk_bf16_f32 v115, v118, v119
	global_store_dwordx4 v[152:153], v[112:115], off offset:256
	v_cvt_f32_i32_e32 v109, v109
	v_cvt_f32_i32_e32 v108, v108
	v_or_b32_e32 v112, 16, v158
	v_lshl_add_u32 v113, v112, 2, s88
	ds_read_b32 v114, v113
	v_cvt_f32_i32_e32 v111, v111
	v_cvt_f32_i32_e32 v110, v110
	v_cvt_f32_i32_e32 v89, v89
	v_cvt_f32_i32_e32 v91, v91
	v_cvt_f32_i32_e32 v90, v90
	v_cvt_f32_i32_e32 v88, v88
	v_or_b32_e32 v115, 32, v158
	s_waitcnt lgkmcnt(0)
	v_pk_mul_f32 v[122:123], v[136:137], v[114:115] op_sel_hi:[1,0]
	v_pk_mul_f32 v[124:125], v[142:143], v[114:115] op_sel_hi:[1,0]
	v_add_u32_e32 v112, s42, v112
	v_pk_mul_f32 v[110:111], v[122:123], v[110:111]
	v_pk_mul_f32 v[108:109], v[124:125], v[108:109]
	v_pk_mul_f32 v[122:123], v[138:139], v[114:115] op_sel_hi:[1,0]
	v_pk_mul_f32 v[124:125], v[140:141], v[114:115] op_sel_hi:[1,0]
	v_mad_i64_i32 v[112:113], s[70:71], v112, s33, v[144:145]
	v_pk_mul_f32 v[122:123], v[122:123], v[90:91]
	v_pk_mul_f32 v[90:91], v[124:125], v[88:89]
	v_lshl_add_u64 v[112:113], v[112:113], 0, v[146:147]
	v_lshl_add_u32 v116, v115, 2, s88
	v_or_b32_e32 v117, 48, v158
	v_cvt_pk_bf16_f32 v88, v108, v109
	v_cvt_pk_bf16_f32 v89, v110, v111
	v_cvt_pk_bf16_f32 v90, v90, v91
	v_cvt_pk_bf16_f32 v91, v122, v123
	v_lshl_add_u32 v119, v117, 2, s88
	ds_read_b32 v118, v116
	ds_read_b32 v116, v119
	ds_read_b32 v120, v151 offset:704
	global_store_dwordx4 v[112:113], v[88:91], off
	s_and_b64 s[98:99], exec, s[44:45]
	s_cbranch_scc0 .Lp1_epi_nobar
	s_barrier
.Lp1_epi_nobar:
	v_cvt_f32_i32_e32 v101, v101
	v_cvt_f32_i32_e32 v103, v103
	v_cvt_f32_i32_e32 v89, v105
	v_cvt_f32_i32_e32 v91, v107
	v_cvt_f32_i32_e32 v90, v106
	v_cvt_f32_i32_e32 v88, v104
	v_cvt_f32_i32_e32 v102, v102
	v_cvt_f32_i32_e32 v100, v100
	v_pk_mul_f32 v[104:105], v[132:133], v[114:115] op_sel_hi:[1,0]
	v_pk_mul_f32 v[106:107], v[134:135], v[114:115] op_sel_hi:[1,0]
	v_pk_mul_f32 v[90:91], v[104:105], v[90:91]
	v_pk_mul_f32 v[88:89], v[106:107], v[88:89]
	v_pk_mul_f32 v[104:105], v[128:129], v[114:115] op_sel_hi:[1,0]
	v_pk_mul_f32 v[106:107], v[130:131], v[114:115] op_sel_hi:[1,0]
	v_cvt_f32_i32_e32 v61, v61
	v_cvt_f32_i32_e32 v63, v63
	v_cvt_f32_i32_e32 v62, v62
	v_cvt_f32_i32_e32 v60, v60
	v_pk_mul_f32 v[102:103], v[104:105], v[102:103]
	v_pk_mul_f32 v[100:101], v[106:107], v[100:101]
	v_cvt_f32_i32_e32 v57, v57
	v_cvt_f32_i32_e32 v59, v59
	v_cvt_f32_i32_e32 v58, v58
	v_cvt_f32_i32_e32 v56, v56
	v_cvt_pk_bf16_f32 v88, v88, v89
	v_cvt_pk_bf16_f32 v89, v90, v91
	v_cvt_pk_bf16_f32 v90, v100, v101
	v_cvt_pk_bf16_f32 v91, v102, v103
	global_store_dwordx4 v[112:113], v[88:91], off offset:256
	s_waitcnt lgkmcnt(2)
	v_pk_mul_f32 v[100:101], v[142:143], v[118:119] op_sel_hi:[1,0]
	v_cvt_f32_i32_e32 v29, v29
	v_pk_mul_f32 v[90:91], v[136:137], v[118:119] op_sel_hi:[1,0]
	v_add_u32_e32 v88, s42, v115
	v_pk_mul_f32 v[62:63], v[90:91], v[62:63]
	v_pk_mul_f32 v[60:61], v[100:101], v[60:61]
	v_pk_mul_f32 v[90:91], v[138:139], v[118:119] op_sel_hi:[1,0]
	v_pk_mul_f32 v[100:101], v[140:141], v[118:119] op_sel_hi:[1,0]
	v_mad_i64_i32 v[88:89], s[70:71], v88, s33, v[144:145]
	v_pk_mul_f32 v[90:91], v[90:91], v[58:59]
	v_pk_mul_f32 v[58:59], v[100:101], v[56:57]
	v_lshl_add_u64 v[88:89], v[88:89], 0, v[146:147]
	v_cvt_pk_bf16_f32 v56, v60, v61
	v_cvt_pk_bf16_f32 v57, v62, v63
	v_cvt_pk_bf16_f32 v58, v58, v59
	v_cvt_pk_bf16_f32 v59, v90, v91
	global_store_dwordx4 v[88:89], v[56:59], off
	v_pk_mul_f32 v[60:61], v[132:133], v[118:119] op_sel_hi:[1,0]
	v_pk_mul_f32 v[62:63], v[134:135], v[118:119] op_sel_hi:[1,0]
	v_cvt_f32_i32_e32 v57, v77
	v_cvt_f32_i32_e32 v59, v79
	v_cvt_f32_i32_e32 v58, v78
	v_cvt_f32_i32_e32 v56, v76
	v_cvt_f32_i32_e32 v31, v31
	v_cvt_f32_i32_e32 v30, v30
	v_pk_mul_f32 v[58:59], v[60:61], v[58:59]
	v_pk_mul_f32 v[56:57], v[62:63], v[56:57]
	v_cvt_f32_i32_e32 v61, v69
	v_cvt_f32_i32_e32 v63, v71
	v_cvt_f32_i32_e32 v62, v70
	v_cvt_f32_i32_e32 v60, v68
	v_pk_mul_f32 v[68:69], v[128:129], v[118:119] op_sel_hi:[1,0]
	v_pk_mul_f32 v[70:71], v[130:131], v[118:119] op_sel_hi:[1,0]
	v_cvt_f32_i32_e32 v28, v28
	v_pk_mul_f32 v[62:63], v[68:69], v[62:63]
	v_pk_mul_f32 v[60:61], v[70:71], v[60:61]
	v_cvt_f32_i32_e32 v25, v25
	v_cvt_f32_i32_e32 v27, v27
	v_cvt_f32_i32_e32 v26, v26
	v_cvt_f32_i32_e32 v24, v24
	v_cvt_pk_bf16_f32 v56, v56, v57
	v_cvt_pk_bf16_f32 v57, v58, v59
	v_cvt_pk_bf16_f32 v58, v60, v61
	v_cvt_pk_bf16_f32 v59, v62, v63
	global_store_dwordx4 v[88:89], v[56:59], off offset:256
	s_waitcnt lgkmcnt(1)
; #define GAS __attribute__((address_space(1)))
; __device__ __forceinline__ unsigned cvt_pk_bf16(float lo, float hi) { const f32x2c v = {lo, hi}; const bf16x2c b = __builtin_convertvector(v, bf16x2c); return __builtin_bit_cast(unsigned, b); }
;     __device__ __forceinline__ void operator()(const i32x4 (&acc)[2][2][4][2], const Unit& u, int wr, int wc, int fr, int fq, PG8_LAS unsigned* scr) const {
;     ...
;             for (int m = 0; m < 4; ++m) { const int r = ai * HALF + wr * 64 + m * 16 + fr; const float rs = __uint_as_float(scr[r]); bf16_t* rowp = O + (size_t)(u.pm * BM + r) * ldc + col0;
; #pragma unroll
;                 for (int bj = 0; bj < 2; ++bj) { const f32x4 v0 = __builtin_convertvector(acc[ai][bj][m][0], f32x4) * (cs[bj][0] * rs), v1 = __builtin_convertvector(acc[ai][bj][m][1], f32x4) * (cs[bj][1] * rs);
;                     u32x4 w; w.x = cvt_pk_bf16(v0[0], v0[1]); w.y = cvt_pk_bf16(v0[2], v0[3]); w.z = cvt_pk_bf16(v1[0], v1[1]); w.w = cvt_pk_bf16(v1[2], v1[3]);
;                     *(GAS u32x4*)(rowp + bj * HALF) = w; } }
	v_pk_mul_f32 v[60:61], v[142:143], v[116:117] op_sel_hi:[1,0]
	v_cvt_f32_i32_e32 v21, v21
	v_pk_mul_f32 v[58:59], v[136:137], v[116:117] op_sel_hi:[1,0]
	v_add_u32_e32 v56, s42, v117
	v_pk_mul_f32 v[30:31], v[58:59], v[30:31]
	v_pk_mul_f32 v[28:29], v[60:61], v[28:29]
	v_pk_mul_f32 v[58:59], v[138:139], v[116:117] op_sel_hi:[1,0]
	v_pk_mul_f32 v[60:61], v[140:141], v[116:117] op_sel_hi:[1,0]
	v_mad_i64_i32 v[56:57], s[42:43], v56, s33, v[144:145]
	v_pk_mul_f32 v[58:59], v[58:59], v[26:27]
	v_pk_mul_f32 v[26:27], v[60:61], v[24:25]
	v_lshl_add_u64 v[56:57], v[56:57], 0, v[146:147]
	v_cvt_pk_bf16_f32 v24, v28, v29
	v_cvt_pk_bf16_f32 v25, v30, v31
	v_cvt_pk_bf16_f32 v26, v26, v27
	v_cvt_pk_bf16_f32 v27, v58, v59
	global_store_dwordx4 v[56:57], v[24:27], off
	v_pk_mul_f32 v[28:29], v[132:133], v[116:117] op_sel_hi:[1,0]
	v_pk_mul_f32 v[30:31], v[134:135], v[116:117] op_sel_hi:[1,0]
	v_cvt_f32_i32_e32 v25, v45
	v_cvt_f32_i32_e32 v27, v47
	v_cvt_f32_i32_e32 v26, v46
	v_cvt_f32_i32_e32 v24, v44
	v_cvt_f32_i32_e32 v20, v20
	v_cvt_f32_i32_e32 v23, v23
	v_pk_mul_f32 v[26:27], v[28:29], v[26:27]
	v_pk_mul_f32 v[24:25], v[30:31], v[24:25]
	v_cvt_f32_i32_e32 v29, v33
	v_cvt_f32_i32_e32 v31, v35
	v_cvt_f32_i32_e32 v30, v34
	v_cvt_f32_i32_e32 v28, v32
	v_pk_mul_f32 v[32:33], v[128:129], v[116:117] op_sel_hi:[1,0]
	v_pk_mul_f32 v[34:35], v[130:131], v[116:117] op_sel_hi:[1,0]
	v_pk_mul_f32 v[30:31], v[32:33], v[30:31]
	v_pk_mul_f32 v[28:29], v[34:35], v[28:29]
	v_cvt_pk_bf16_f32 v24, v24, v25
	v_cvt_pk_bf16_f32 v25, v26, v27
	v_cvt_pk_bf16_f32 v26, v28, v29
	v_cvt_pk_bf16_f32 v27, v30, v31
	global_store_dwordx4 v[56:57], v[24:27], off offset:256
	v_mov_b32_e32 v30, v149
	v_pk_mul_f32 v[32:33], v[136:137], v[30:31] op_sel_hi:[1,0]
	v_add_u32_e32 v24, 0x80, v150
	v_mad_i64_i32 v[24:25], s[42:43], v24, s33, v[144:145]
	v_lshl_add_u64 v[28:29], v[24:25], 0, v[146:147]
	v_cvt_f32_i32_e32 v25, v85
	v_cvt_f32_i32_e32 v24, v84
	v_cvt_f32_i32_e32 v27, v87
	v_cvt_f32_i32_e32 v26, v86
	v_pk_mul_f32 v[34:35], v[142:143], v[30:31] op_sel_hi:[1,0]
	v_pk_mul_f32 v[44:45], v[138:139], v[30:31] op_sel_hi:[1,0]
	v_pk_mul_f32 v[24:25], v[34:35], v[24:25]
	v_pk_mul_f32 v[26:27], v[32:33], v[26:27]
	v_cvt_f32_i32_e32 v33, v81
	v_cvt_f32_i32_e32 v35, v83
	v_cvt_f32_i32_e32 v34, v82
	v_cvt_f32_i32_e32 v32, v80
	v_pk_mul_f32 v[46:47], v[140:141], v[30:31] op_sel_hi:[1,0]
	v_cvt_pk_bf16_f32 v24, v24, v25
	v_pk_mul_f32 v[34:35], v[44:45], v[34:35]
	v_pk_mul_f32 v[32:33], v[46:47], v[32:33]
	v_cvt_pk_bf16_f32 v25, v26, v27
	v_cvt_pk_bf16_f32 v26, v32, v33
	v_cvt_pk_bf16_f32 v27, v34, v35
	global_store_dwordx4 v[28:29], v[24:27], off
	v_pk_mul_f32 v[32:33], v[132:133], v[30:31] op_sel_hi:[1,0]
	v_pk_mul_f32 v[34:35], v[134:135], v[30:31] op_sel_hi:[1,0]
	v_cvt_f32_i32_e32 v25, v97
	v_cvt_f32_i32_e32 v27, v99
	v_cvt_f32_i32_e32 v26, v98
	v_cvt_f32_i32_e32 v24, v96
	v_pk_mul_f32 v[44:45], v[128:129], v[30:31] op_sel_hi:[1,0]
	v_pk_mul_f32 v[30:31], v[130:131], v[30:31] op_sel_hi:[1,0]
	v_pk_mul_f32 v[26:27], v[32:33], v[26:27]
	v_pk_mul_f32 v[24:25], v[34:35], v[24:25]
	v_cvt_f32_i32_e32 v33, v93
	v_cvt_f32_i32_e32 v35, v95
	v_cvt_f32_i32_e32 v34, v94
	v_cvt_f32_i32_e32 v32, v92
	v_cvt_pk_bf16_f32 v24, v24, v25
	v_cvt_pk_bf16_f32 v25, v26, v27
	v_pk_mul_f32 v[34:35], v[44:45], v[34:35]
	v_pk_mul_f32 v[30:31], v[30:31], v[32:33]
	v_cvt_pk_bf16_f32 v27, v34, v35
	v_cvt_pk_bf16_f32 v26, v30, v31
	global_store_dwordx4 v[28:29], v[24:27], off offset:256
	ds_read2_b32 v[28:29], v151 offset0:144 offset1:160
	v_cvt_f32_i32_e32 v22, v22
	v_add_u32_e32 v24, 0x90, v150
	v_mad_i64_i32 v[24:25], s[42:43], v24, s33, v[144:145]
	v_lshl_add_u64 v[30:31], v[24:25], 0, v[146:147]
	v_cvt_f32_i32_e32 v25, v53
	v_cvt_f32_i32_e32 v27, v55
	v_cvt_f32_i32_e32 v26, v54
	v_cvt_f32_i32_e32 v24, v52
	s_waitcnt lgkmcnt(0)
; #define GAS __attribute__((address_space(1)))
; __device__ __forceinline__ unsigned cvt_pk_bf16(float lo, float hi) { const f32x2c v = {lo, hi}; const bf16x2c b = __builtin_convertvector(v, bf16x2c); return __builtin_bit_cast(unsigned, b); }
; #define PG8_BAR __builtin_amdgcn_s_barrier()
;     __device__ __forceinline__ void operator()(const i32x4 (&acc)[2][2][4][2], const Unit& u, int wr, int wc, int fr, int fq, PG8_LAS unsigned* scr) const {
;     ...
;             for (int m = 0; m < 4; ++m) { const int r = ai * HALF + wr * 64 + m * 16 + fr; const float rs = __uint_as_float(scr[r]); bf16_t* rowp = O + (size_t)(u.pm * BM + r) * ldc + col0;
; #pragma unroll
;                 for (int bj = 0; bj < 2; ++bj) { const f32x4 v0 = __builtin_convertvector(acc[ai][bj][m][0], f32x4) * (cs[bj][0] * rs), v1 = __builtin_convertvector(acc[ai][bj][m][1], f32x4) * (cs[bj][1] * rs);
;                     u32x4 w; w.x = cvt_pk_bf16(v0[0], v0[1]); w.y = cvt_pk_bf16(v0[2], v0[3]); w.z = cvt_pk_bf16(v1[0], v1[1]); w.w = cvt_pk_bf16(v1[2], v1[3]);
;                     *(GAS u32x4*)(rowp + bj * HALF) = w; } }
; template <class Epi, class Sched, bool GATHER, int MODE>
; __device__ __forceinline__ void gemm_phase(PG8_LAS unsigned char* lds, PG8_LAS unsigned* scr, const Gemm g, const Sched& S, const Epi& E, int tid_in) {
;     ...
;         if (!has_next) break;
;         cur = nxt; cA = nA; cB = nB; ++ui;
;         if (GATHER) { const u32x4 nx = gather_read(cur); c0[0] = nx[0]; c0[1] = nx[1]; c1[0] = nx[2]; c1[1] = nx[3]; }
;         if (wr == 1) PG8_BAR;
	v_pk_mul_f32 v[32:33], v[136:137], v[28:29] op_sel_hi:[1,0]
	v_pk_mul_f32 v[34:35], v[142:143], v[28:29] op_sel_hi:[1,0]
	v_pk_mul_f32 v[26:27], v[32:33], v[26:27]
	v_pk_mul_f32 v[24:25], v[34:35], v[24:25]
	v_cvt_f32_i32_e32 v33, v49
	v_cvt_f32_i32_e32 v35, v51
	v_cvt_f32_i32_e32 v34, v50
	v_cvt_f32_i32_e32 v32, v48
	v_pk_mul_f32 v[44:45], v[138:139], v[28:29] op_sel_hi:[1,0]
	v_pk_mul_f32 v[46:47], v[140:141], v[28:29] op_sel_hi:[1,0]
	v_pk_mul_f32 v[34:35], v[44:45], v[34:35]
	v_pk_mul_f32 v[32:33], v[46:47], v[32:33]
	v_cvt_pk_bf16_f32 v24, v24, v25
	v_cvt_pk_bf16_f32 v25, v26, v27
	v_cvt_pk_bf16_f32 v26, v32, v33
	v_cvt_pk_bf16_f32 v27, v34, v35
	global_store_dwordx4 v[30:31], v[24:27], off
	v_pk_mul_f32 v[32:33], v[132:133], v[28:29] op_sel_hi:[1,0]
	v_pk_mul_f32 v[34:35], v[134:135], v[28:29] op_sel_hi:[1,0]
	v_cvt_f32_i32_e32 v25, v73
	v_cvt_f32_i32_e32 v27, v75
	v_cvt_f32_i32_e32 v26, v74
	v_cvt_f32_i32_e32 v24, v72
	v_pk_mul_f32 v[44:45], v[128:129], v[28:29] op_sel_hi:[1,0]
	v_pk_mul_f32 v[46:47], v[130:131], v[28:29] op_sel_hi:[1,0]
	v_pk_mul_f32 v[26:27], v[32:33], v[26:27]
	v_pk_mul_f32 v[24:25], v[34:35], v[24:25]
	v_cvt_f32_i32_e32 v33, v65
	v_cvt_f32_i32_e32 v35, v67
	v_cvt_f32_i32_e32 v34, v66
	v_cvt_f32_i32_e32 v32, v64
	v_cvt_pk_bf16_f32 v24, v24, v25
	v_cvt_pk_bf16_f32 v25, v26, v27
	v_pk_mul_f32 v[34:35], v[44:45], v[34:35]
	v_pk_mul_f32 v[32:33], v[46:47], v[32:33]
	v_cvt_pk_bf16_f32 v27, v34, v35
	v_cvt_pk_bf16_f32 v26, v32, v33
	v_cvt_f32_i32_e32 v17, v17
	v_cvt_f32_i32_e32 v19, v19
	v_cvt_f32_i32_e32 v18, v18
	v_cvt_f32_i32_e32 v16, v16
	global_store_dwordx4 v[30:31], v[24:27], off offset:256
	v_cvt_f32_i32_e32 v9, v9
	v_cvt_f32_i32_e32 v11, v11
	v_mov_b32_e32 v26, v29
	v_pk_mul_f32 v[28:29], v[136:137], v[26:27] op_sel_hi:[1,0]
	v_pk_mul_f32 v[30:31], v[142:143], v[26:27] op_sel_hi:[1,0]
	v_add_u32_e32 v24, 0xa0, v150
	v_pk_mul_f32 v[22:23], v[28:29], v[22:23]
	v_pk_mul_f32 v[20:21], v[30:31], v[20:21]
	v_pk_mul_f32 v[28:29], v[138:139], v[26:27] op_sel_hi:[1,0]
	v_pk_mul_f32 v[30:31], v[140:141], v[26:27] op_sel_hi:[1,0]
	v_mad_i64_i32 v[24:25], s[42:43], v24, s33, v[144:145]
	v_pk_mul_f32 v[28:29], v[28:29], v[18:19]
	v_pk_mul_f32 v[18:19], v[30:31], v[16:17]
	v_lshl_add_u64 v[24:25], v[24:25], 0, v[146:147]
	v_cvt_pk_bf16_f32 v16, v20, v21
	v_cvt_pk_bf16_f32 v17, v22, v23
	v_cvt_pk_bf16_f32 v18, v18, v19
	v_cvt_pk_bf16_f32 v19, v28, v29
	global_store_dwordx4 v[24:25], v[16:19], off
	v_pk_mul_f32 v[20:21], v[132:133], v[26:27] op_sel_hi:[1,0]
	v_pk_mul_f32 v[22:23], v[134:135], v[26:27] op_sel_hi:[1,0]
	v_cvt_f32_i32_e32 v17, v41
	v_cvt_f32_i32_e32 v19, v43
	v_cvt_f32_i32_e32 v18, v42
	v_cvt_f32_i32_e32 v16, v40
	v_pk_mul_f32 v[28:29], v[128:129], v[26:27] op_sel_hi:[1,0]
	v_pk_mul_f32 v[26:27], v[130:131], v[26:27] op_sel_hi:[1,0]
	v_pk_mul_f32 v[18:19], v[20:21], v[18:19]
	v_pk_mul_f32 v[16:17], v[22:23], v[16:17]
	v_cvt_f32_i32_e32 v21, v37
	v_cvt_f32_i32_e32 v23, v39
	v_cvt_f32_i32_e32 v22, v38
	v_cvt_f32_i32_e32 v20, v36
	v_cvt_f32_i32_e32 v10, v10
	v_cvt_f32_i32_e32 v8, v8
	v_pk_mul_f32 v[22:23], v[28:29], v[22:23]
	v_pk_mul_f32 v[20:21], v[26:27], v[20:21]
	v_cvt_f32_i32_e32 v1, v1
	v_cvt_f32_i32_e32 v3, v3
	v_cvt_f32_i32_e32 v2, v2
	v_cvt_f32_i32_e32 v0, v0
	v_cvt_pk_bf16_f32 v16, v16, v17
	v_cvt_pk_bf16_f32 v17, v18, v19
	v_cvt_pk_bf16_f32 v18, v20, v21
	v_cvt_pk_bf16_f32 v19, v22, v23
	global_store_dwordx4 v[24:25], v[16:19], off offset:256
	v_pk_mul_f32 v[20:21], v[142:143], v[120:121] op_sel_hi:[1,0]
	v_cvt_f32_i32_e32 v5, v5
	v_pk_mul_f32 v[18:19], v[136:137], v[120:121] op_sel_hi:[1,0]
	v_add_u32_e32 v16, 0xb0, v150
	v_pk_mul_f32 v[10:11], v[18:19], v[10:11]
	v_pk_mul_f32 v[8:9], v[20:21], v[8:9]
	v_pk_mul_f32 v[18:19], v[138:139], v[120:121] op_sel_hi:[1,0]
	v_pk_mul_f32 v[20:21], v[140:141], v[120:121] op_sel_hi:[1,0]
	v_mad_i64_i32 v[16:17], s[42:43], v16, s33, v[144:145]
	v_pk_mul_f32 v[18:19], v[18:19], v[2:3]
	v_pk_mul_f32 v[2:3], v[20:21], v[0:1]
	v_lshl_add_u64 v[16:17], v[16:17], 0, v[146:147]
	v_cvt_pk_bf16_f32 v0, v8, v9
	v_cvt_pk_bf16_f32 v1, v10, v11
	v_cvt_pk_bf16_f32 v2, v2, v3
	v_cvt_pk_bf16_f32 v3, v18, v19
	global_store_dwordx4 v[16:17], v[0:3], off
	v_cvt_f32_i32_e32 v7, v7
	v_cvt_f32_i32_e32 v6, v6
	v_cvt_f32_i32_e32 v1, v13
	v_cvt_f32_i32_e32 v3, v15
	v_cvt_f32_i32_e32 v2, v14
	v_cvt_f32_i32_e32 v0, v12
	v_cvt_f32_i32_e32 v4, v4
	v_pk_mul_f32 v[8:9], v[132:133], v[120:121] op_sel_hi:[1,0]
	v_pk_mul_f32 v[10:11], v[134:135], v[120:121] op_sel_hi:[1,0]
	v_pk_mul_f32 v[2:3], v[8:9], v[2:3]
	v_pk_mul_f32 v[0:1], v[10:11], v[0:1]
	v_pk_mul_f32 v[8:9], v[128:129], v[120:121] op_sel_hi:[1,0]
	v_pk_mul_f32 v[10:11], v[130:131], v[120:121] op_sel_hi:[1,0]
	v_pk_mul_f32 v[6:7], v[8:9], v[6:7]
	v_pk_mul_f32 v[4:5], v[10:11], v[4:5]
	v_cvt_pk_bf16_f32 v0, v0, v1
	v_cvt_pk_bf16_f32 v1, v2, v3
	v_cvt_pk_bf16_f32 v2, v4, v5
	v_cvt_pk_bf16_f32 v3, v6, v7
	s_andn2_b64 vcc, exec, s[36:37]
	s_mov_b64 s[36:37], -1
	global_store_dwordx4 v[16:17], v[0:3], off offset:256
	s_cbranch_vccnz .LBB0_336
	s_andn2_b64 vcc, exec, s[10:11]
	s_cbranch_vccnz .LBB0_335
	s_barrier
	s_branch .LBB0_335

; #define PG8_STAGE(bufoff, base, uoff, voff) do { _Pragma("unroll") for (int _i = 0; _i < 2; ++_i) \
;         __builtin_amdgcn_raw_ptr_buffer_load_lds((base), (PG8_LAS void*)(lds + (bufoff) + ldsw + _i * 8192), 16, (int)(voff)[_i], (int)(uoff), 0, 0); } while (0)
; #define PG8_LDA(dst, b, h) do { _Pragma("unroll") for (int m = 0; m < 4; ++m) _Pragma("unroll") for (int k = 0; k < 2; ++k) dst[m][k] = *(const PG8_LAS bf16x8*)(lds + PG8_SA(b, h) + aoff + m * 2048 + k * 1024); } while (0)
; #define PG8_LDB(dst, b, h) do { _Pragma("unroll") for (int n = 0; n < 2; ++n) _Pragma("unroll") for (int k = 0; k < 2; ++k) dst[n][k] = *(const PG8_LAS bf16x8*)(lds + PG8_SB(b, h) + boff + n * 2048 + k * 1024); } while (0)
; #define PG8_WAIT_V(n) asm volatile("s_waitcnt vmcnt(" #n ")" ::: "memory")
; template <class Epi, class Sched, bool GATHER, int MODE>
; __device__ __forceinline__ void gemm_phase(PG8_LAS unsigned char* lds, PG8_LAS unsigned* scr, const Gemm g, const Sched& S, const Epi& E, int tid_in) {
;     ...
;             const int tt = __builtin_amdgcn_readfirstlane(t);
;             const unsigned a1 = cA + (unsigned)(tt + 1) * kstep;
;             const unsigned a2 = last ? nA : cA + (unsigned)(tt + 2) * kstep, b2 = last ? nB : cB + (unsigned)(tt + 2) * kstep;
;             const unsigned a3 = a2 + kstep, b3 = b2 + kstep;
;             unsigned s0[2], s1[2];
;             if (GATHER && last && has_next) { const u32x4 nx = gather_read(nxt); s0[0] = nx[0]; s0[1] = nx[1]; s1[0] = nx[2]; s1[1] = nx[3]; }
;             else { s0[0] = c0[0]; s0[1] = c0[1]; s1[0] = c1[0]; s1[1] = c1[1]; }
;             PG8_LDB(B0, 0, 0); PG8_LDB(B1, 0, 1); PG8_SCHED; PG8_LDA(At, 0, 0); PG8_STAGE(PG8_SA(1, 1), baseA, a1 + hstepA, c1);
;             PG8_WAIT_V(8); PG8_WAIT_L(0); PG8_BAR; PG8_MMA(0, 0, At, B0); PG8_MMA(0, 1, At, B1); PG8_BAR; PG8_SCHED;
;             PG8_LDA(At, 0, 1); PG8_STAGE(PG8_SB(0, 0), baseB, b2, voffB); PG8_STAGE(PG8_SB(0, 1), baseB, b2 + hstep, voffB); PG8_STAGE(PG8_SA(0, 0), baseA, a2, s0);
;             PG8_WAIT_V(8); PG8_WAIT_L(0); PG8_BAR; PG8_MMA(1, 0, At, B0); PG8_MMA(1, 1, At, B1); PG8_BAR; PG8_SCHED;
;             PG8_LDB(B0, 1, 0); PG8_LDB(B1, 1, 1); PG8_SCHED; PG8_LDA(At, 1, 0); PG8_STAGE(PG8_SA(0, 1), baseA, a2 + hstepA, s1);
;             PG8_WAIT_V(8); PG8_WAIT_L(0); PG8_BAR; PG8_MMA(0, 0, At, B0); PG8_MMA(0, 1, At, B1); PG8_BAR; PG8_SCHED;
.LBB0_958:
	ds_read_b128 v[0:3], v208
	ds_read_b128 v[4:7], v208 offset:1024
	ds_read_b128 v[8:11], v208 offset:2048
	ds_read_b128 v[12:15], v208 offset:3072
	ds_read_b128 v[16:19], v209
	ds_read_b128 v[20:23], v209 offset:1024
	ds_read_b128 v[24:27], v209 offset:2048
	ds_read_b128 v[28:31], v209 offset:3072
	s_add_i32 s80, s81, 2
	s_lshl_b32 s84, s80, 7
	s_add_i32 s82, s84, 0x100
	s_add_i32 s83, s82, s77
	s_add_i32 s82, s82, s78
	s_cmp_eq_u32 s81, 4
	s_cselect_b32 s83, s36, s83
	s_cselect_b32 s82, s37, s82
	s_add_i32 s81, s83, 0x80
	s_add_i32 s84, s84, s79
	s_mov_b32 m0, s66
	ds_read_b128 v[210:213], v206
	ds_read_b128 v[214:217], v206 offset:1024
	ds_read_b128 v[218:221], v206 offset:2048
	ds_read_b128 v[222:225], v206 offset:3072
	ds_read_b128 v[226:229], v206 offset:4096
	ds_read_b128 v[230:233], v206 offset:5120
	ds_read_b128 v[242:245], v206 offset:6144
	ds_read_b128 v[246:249], v206 offset:7168
	buffer_load_dwordx4 v181, s[4:7], s84 offen lds
	s_mov_b32 m0, s68
	s_nop 0
	buffer_load_dwordx4 v202, s[4:7], s84 offen lds
	s_waitcnt vmcnt(8)
	s_waitcnt lgkmcnt(0)
	s_barrier
	s_setprio 1
	s_waitcnt lgkmcnt(6)
	v_mfma_f32_16x16x128_f8f6f4 v[152:155], v[0:7], v[210:217], v[152:155]
	v_mfma_f32_16x16x128_f8f6f4 v[156:159], v[8:15], v[210:217], v[156:159]
	s_waitcnt lgkmcnt(4)
	v_mfma_f32_16x16x128_f8f6f4 v[140:143], v[0:7], v[218:225], v[140:143]
	v_mfma_f32_16x16x128_f8f6f4 v[136:139], v[8:15], v[218:225], v[136:139]
	s_waitcnt lgkmcnt(2)
	v_mfma_f32_16x16x128_f8f6f4 v[132:135], v[0:7], v[226:233], v[132:135]
	v_mfma_f32_16x16x128_f8f6f4 v[124:127], v[8:15], v[226:233], v[124:127]
	s_waitcnt lgkmcnt(0)
	v_mfma_f32_16x16x128_f8f6f4 v[116:119], v[0:7], v[242:249], v[116:119]
	v_mfma_f32_16x16x128_f8f6f4 v[108:111], v[8:15], v[242:249], v[108:111]
	s_setprio 0
	s_setprio 1
	v_mfma_f32_16x16x128_f8f6f4 v[160:163], v[16:23], v[210:217], v[160:163]
	v_mfma_f32_16x16x128_f8f6f4 v[164:167], v[24:31], v[210:217], v[164:167]
	v_mfma_f32_16x16x128_f8f6f4 v[148:151], v[16:23], v[218:225], v[148:151]
	v_mfma_f32_16x16x128_f8f6f4 v[144:147], v[24:31], v[218:225], v[144:147]
	v_mfma_f32_16x16x128_f8f6f4 v[128:131], v[16:23], v[226:233], v[128:131]
	v_mfma_f32_16x16x128_f8f6f4 v[120:123], v[24:31], v[226:233], v[120:123]
	v_mfma_f32_16x16x128_f8f6f4 v[112:115], v[16:23], v[242:249], v[112:115]
	v_mfma_f32_16x16x128_f8f6f4 v[104:107], v[24:31], v[242:249], v[104:107]
	s_setprio 0
	s_barrier
	s_mov_b32 m0, s49
	ds_read_b128 v[210:213], v206 offset:16384
	ds_read_b128 v[214:217], v206 offset:17408
	ds_read_b128 v[218:221], v206 offset:18432
	ds_read_b128 v[222:225], v206 offset:19456
	ds_read_b128 v[226:229], v206 offset:20480
	ds_read_b128 v[230:233], v206 offset:21504
	ds_read_b128 v[242:245], v206 offset:22528
	ds_read_b128 v[246:249], v206 offset:23552
	buffer_load_dwordx4 v201, s[40:43], s82 offen lds
	s_mov_b32 m0, s50
	s_add_i32 s84, s82, 0x20000
	buffer_load_dwordx4 v203, s[40:43], s82 offen lds
	s_mov_b32 m0, s51
	s_nop 0
	buffer_load_dwordx4 v201, s[40:43], s84 offen lds
	s_mov_b32 m0, s52
	s_nop 0
	buffer_load_dwordx4 v203, s[40:43], s84 offen lds
	s_mov_b32 m0, s48
	s_nop 0
	buffer_load_dwordx4 v181, s[4:7], s83 offen lds
	s_mov_b32 m0, s53
	s_nop 0
	buffer_load_dwordx4 v202, s[4:7], s83 offen lds
	s_waitcnt vmcnt(8)
	s_waitcnt lgkmcnt(0)
	s_barrier
	s_setprio 1
	s_waitcnt lgkmcnt(6)
	v_mfma_f32_16x16x128_f8f6f4 v[96:99], v[0:7], v[210:217], v[96:99]
	v_mfma_f32_16x16x128_f8f6f4 v[88:91], v[8:15], v[210:217], v[88:91]
	s_waitcnt lgkmcnt(4)
	v_mfma_f32_16x16x128_f8f6f4 v[84:87], v[0:7], v[218:225], v[84:87]
	v_mfma_f32_16x16x128_f8f6f4 v[80:83], v[8:15], v[218:225], v[80:83]
	s_waitcnt lgkmcnt(2)
	v_mfma_f32_16x16x128_f8f6f4 v[72:75], v[0:7], v[226:233], v[72:75]
	v_mfma_f32_16x16x128_f8f6f4 v[76:79], v[8:15], v[226:233], v[76:79]
	s_waitcnt lgkmcnt(0)
	v_mfma_f32_16x16x128_f8f6f4 v[68:71], v[0:7], v[242:249], v[68:71]
	v_mfma_f32_16x16x128_f8f6f4 v[64:67], v[8:15], v[242:249], v[64:67]
	s_setprio 0
	s_setprio 1
	v_mfma_f32_16x16x128_f8f6f4 v[100:103], v[16:23], v[210:217], v[100:103]
	v_mfma_f32_16x16x128_f8f6f4 v[92:95], v[24:31], v[210:217], v[92:95]
	v_mfma_f32_16x16x128_f8f6f4 v[60:63], v[16:23], v[218:225], v[60:63]
	v_mfma_f32_16x16x128_f8f6f4 v[56:59], v[24:31], v[218:225], v[56:59]
	v_mfma_f32_16x16x128_f8f6f4 v[48:51], v[16:23], v[226:233], v[48:51]
	v_mfma_f32_16x16x128_f8f6f4 v[52:55], v[24:31], v[226:233], v[52:55]
	v_mfma_f32_16x16x128_f8f6f4 v[44:47], v[16:23], v[242:249], v[44:47]
	v_mfma_f32_16x16x128_f8f6f4 v[40:43], v[24:31], v[242:249], v[40:43]
	s_setprio 0
	s_barrier
	ds_read_b128 v[16:19], v32
	ds_read_b128 v[20:23], v32 offset:1024
	ds_read_b128 v[24:27], v32 offset:2048
	ds_read_b128 v[28:31], v32 offset:3072
	ds_read_b128 v[8:11], v33
	ds_read_b128 v[12:15], v33 offset:1024
	ds_read_b128 v[0:3], v33 offset:2048
	ds_read_b128 v[4:7], v33 offset:3072
	s_add_i32 s83, s83, 0x20000
	s_mov_b32 m0, s54
	ds_read_b128 v[210:213], v206 offset:32768
	ds_read_b128 v[214:217], v206 offset:33792
	ds_read_b128 v[218:221], v206 offset:34816
	ds_read_b128 v[222:225], v206 offset:35840
	ds_read_b128 v[226:229], v206 offset:36864
	ds_read_b128 v[230:233], v206 offset:37888
	ds_read_b128 v[242:245], v206 offset:38912
	ds_read_b128 v[246:249], v206 offset:39936
	buffer_load_dwordx4 v181, s[4:7], s83 offen lds
	s_mov_b32 m0, s55
	s_nop 0
	buffer_load_dwordx4 v202, s[4:7], s83 offen lds
	s_waitcnt vmcnt(8)
	s_waitcnt lgkmcnt(0)
	s_barrier
	s_setprio 1
	s_waitcnt lgkmcnt(6)
	v_mfma_f32_16x16x128_f8f6f4 v[152:155], v[16:23], v[210:217], v[152:155]
	v_mfma_f32_16x16x128_f8f6f4 v[156:159], v[24:31], v[210:217], v[156:159]
	s_waitcnt lgkmcnt(4)
	v_mfma_f32_16x16x128_f8f6f4 v[140:143], v[16:23], v[218:225], v[140:143]
	v_mfma_f32_16x16x128_f8f6f4 v[136:139], v[24:31], v[218:225], v[136:139]
	s_waitcnt lgkmcnt(2)
	v_mfma_f32_16x16x128_f8f6f4 v[132:135], v[16:23], v[226:233], v[132:135]
	v_mfma_f32_16x16x128_f8f6f4 v[124:127], v[24:31], v[226:233], v[124:127]
	s_waitcnt lgkmcnt(0)
	v_mfma_f32_16x16x128_f8f6f4 v[116:119], v[16:23], v[242:249], v[116:119]
	v_mfma_f32_16x16x128_f8f6f4 v[108:111], v[24:31], v[242:249], v[108:111]
	s_setprio 0
	s_setprio 1
	v_mfma_f32_16x16x128_f8f6f4 v[160:163], v[8:15], v[210:217], v[160:163]
	v_mfma_f32_16x16x128_f8f6f4 v[164:167], v[0:7], v[210:217], v[164:167]
	v_mfma_f32_16x16x128_f8f6f4 v[148:151], v[8:15], v[218:225], v[148:151]
	v_mfma_f32_16x16x128_f8f6f4 v[144:147], v[0:7], v[218:225], v[144:147]
	v_mfma_f32_16x16x128_f8f6f4 v[128:131], v[8:15], v[226:233], v[128:131]
	v_mfma_f32_16x16x128_f8f6f4 v[120:123], v[0:7], v[226:233], v[120:123]
	v_mfma_f32_16x16x128_f8f6f4 v[112:115], v[8:15], v[242:249], v[112:115]
	v_mfma_f32_16x16x128_f8f6f4 v[104:107], v[0:7], v[242:249], v[104:107]
	s_setprio 0
	s_barrier
	s_cmp_eq_u32 s80, 6
	s_cbranch_scc0 .Lp6_nostash
	ds_write2st64_b32 v204, v207, v168 offset1:8
; #define PG8_LAS __attribute__((address_space(3)))
; #define PG8_STAGE(bufoff, base, uoff, voff) do { _Pragma("unroll") for (int _i = 0; _i < 2; ++_i) \
;         __builtin_amdgcn_raw_ptr_buffer_load_lds((base), (PG8_LAS void*)(lds + (bufoff) + ldsw + _i * 8192), 16, (int)(voff)[_i], (int)(uoff), 0, 0); } while (0)
; #define PG8_WAIT_V(n) asm volatile("s_waitcnt vmcnt(" #n ")" ::: "memory")
;     __device__ __forceinline__ void operator()(const f32x4 (&acc)[2][2][4][2], const Unit& u, int wr, int wc, int fr, int fq, PG8_LAS unsigned* scr) const {
;         const int jn = u.pn & 3;
;         const int c0 = jn * 256 + wc * 32 + 8 * fq, cl = wc * 32 + 8 * fq;
;         f32x4 bv[2][2], cs[2][2];
; #pragma unroll
;         for (int bj = 0; bj < 2; ++bj)
; #pragma unroll
;             for (int n = 0; n < 2; ++n) { bv[bj][n] = *(const PG8_LAS f32x4*)(scr + 256 + bj * HALF + cl + 4 * n); cs[bj][n] = *(const PG8_LAS f32x4*)(scr + 768 + bj * HALF + cl + 4 * n) * (1.0f / (WDN_SC * ACT_SC)); }
; #pragma unroll
;         for (int ai = 0; ai < 2; ++ai)
; #pragma unroll
;             for (int mp = 0; mp < 4; mp += 2) { unsigned wq[2][2][2]; int dsts[2];
; #pragma unroll
;                 for (int hm = 0; hm < 2; ++hm) { const int m = mp + hm; const int r = ai * HALF + wr * 64 + m * 16 + fr; const int pos = u.rb * 256 + r;
;                     dsts[hm] = pos < u.cnt ? (int)scr[r] : trash + r; const float rg = __uint_as_float(scr[512 + r]) * 16.0f;
; #pragma unroll
;                     for (int bj = 0; bj < 2; ++bj) { f32x4 v0 = (acc[ai][bj][m][0] * cs[bj][0] + bv[bj][0]) * rg, v1 = (acc[ai][bj][m][1] * cs[bj][1] + bv[bj][1]) * rg;
; #pragma unroll
;                         for (int q = 0; q < 4; ++q) { v0[q] = fminf(fmaxf(v0[q], -448.0f), 448.0f); v1[q] = fminf(fmaxf(v1[q], -448.0f), 448.0f); }
; template <class Epi, class Sched, bool GATHER, int MODE>
; __device__ __forceinline__ void gemm_phase(PG8_LAS unsigned char* lds, PG8_LAS unsigned* scr, const Gemm g, const Sched& S, const Epi& E, int tid_in) {
;     ...
;             PG8_LDA(At, 1, 1); PG8_STAGE(PG8_SB(1, 0), baseB, b3, voffB); PG8_STAGE(PG8_SB(1, 1), baseB, b3 + hstep, voffB); PG8_STAGE(PG8_SA(1, 0), baseA, a3, s0);
;             PG8_WAIT_V(8); PG8_WAIT_L(0); PG8_BAR; PG8_MMA(1, 0, At, B0); PG8_MMA(1, 1, At, B1); PG8_BAR; PG8_SCHED;
;         }
;         asm volatile("s_nop 15\n\ts_nop 7" ::: "memory");
.Lp6_nostash:
	s_mov_b32 m0, s60
	s_add_i32 s83, s82, 0x80
	ds_read_b128 v[210:213], v206 offset:49152
	ds_read_b128 v[214:217], v206 offset:50176
	ds_read_b128 v[218:221], v206 offset:51200
	ds_read_b128 v[222:225], v206 offset:52224
	ds_read_b128 v[226:229], v206 offset:53248
	ds_read_b128 v[230:233], v206 offset:54272
	ds_read_b128 v[242:245], v206 offset:55296
	ds_read_b128 v[246:249], v206 offset:56320
	buffer_load_dwordx4 v201, s[40:43], s83 offen lds
	s_mov_b32 m0, s61
	s_add_i32 s82, s82, 0x20080
	buffer_load_dwordx4 v203, s[40:43], s83 offen lds
	s_mov_b32 m0, s64
	s_nop 0
	buffer_load_dwordx4 v201, s[40:43], s82 offen lds
	s_mov_b32 m0, s65
	s_nop 0
	buffer_load_dwordx4 v203, s[40:43], s82 offen lds
	s_mov_b32 m0, s62
	s_nop 0
	buffer_load_dwordx4 v181, s[4:7], s81 offen lds
	s_mov_b32 m0, s63
	s_nop 0
	buffer_load_dwordx4 v202, s[4:7], s81 offen lds
	s_waitcnt vmcnt(8)
	s_waitcnt lgkmcnt(0)
	s_barrier
	s_setprio 1
	s_waitcnt lgkmcnt(6)
	v_mfma_f32_16x16x128_f8f6f4 v[96:99], v[16:23], v[210:217], v[96:99]
	v_mfma_f32_16x16x128_f8f6f4 v[88:91], v[24:31], v[210:217], v[88:91]
	s_waitcnt lgkmcnt(4)
	v_mfma_f32_16x16x128_f8f6f4 v[84:87], v[16:23], v[218:225], v[84:87]
	v_mfma_f32_16x16x128_f8f6f4 v[80:83], v[24:31], v[218:225], v[80:83]
	s_waitcnt lgkmcnt(2)
	v_mfma_f32_16x16x128_f8f6f4 v[72:75], v[16:23], v[226:233], v[72:75]
	v_mfma_f32_16x16x128_f8f6f4 v[76:79], v[24:31], v[226:233], v[76:79]
	s_waitcnt lgkmcnt(0)
	v_mfma_f32_16x16x128_f8f6f4 v[68:71], v[16:23], v[242:249], v[68:71]
	v_mfma_f32_16x16x128_f8f6f4 v[64:67], v[24:31], v[242:249], v[64:67]
	s_setprio 0
	s_setprio 1
	v_mfma_f32_16x16x128_f8f6f4 v[100:103], v[8:15], v[210:217], v[100:103]
	v_mfma_f32_16x16x128_f8f6f4 v[92:95], v[0:7], v[210:217], v[92:95]
	v_mfma_f32_16x16x128_f8f6f4 v[60:63], v[8:15], v[218:225], v[60:63]
	v_mfma_f32_16x16x128_f8f6f4 v[56:59], v[0:7], v[218:225], v[56:59]
	v_mfma_f32_16x16x128_f8f6f4 v[48:51], v[8:15], v[226:233], v[48:51]
	v_mfma_f32_16x16x128_f8f6f4 v[52:55], v[0:7], v[226:233], v[52:55]
	v_mfma_f32_16x16x128_f8f6f4 v[44:47], v[8:15], v[242:249], v[44:47]
	v_mfma_f32_16x16x128_f8f6f4 v[40:43], v[0:7], v[242:249], v[40:43]
	s_setprio 0
	s_barrier
	s_cmp_gt_u32 s80, 5
	s_mov_b32 s81, s80
	s_cbranch_scc0 .LBB0_958
	s_nop 15
	s_nop 7
.LBB0_961:
	v_mov_b32_e32 v168, v182
	s_movk_i32 s36, 0xffc0
	v_lshlrev_b32_e32 v0, 1, v168
	v_and_b32_e32 v0, 0x1e0, v0
	v_add_u32_e32 v0, 0, v0
	v_add_u32_e32 v1, 0x20d00, v0
	v_add_u32_e32 v16, 0x21500, v0
	ds_read_b128 v[12:15], v1
	ds_read_b128 v[8:11], v1 offset:16
	ds_read_b128 v[28:31], v16
	ds_read_b128 v[20:23], v16 offset:16
	ds_read_b128 v[4:7], v1 offset:512
	ds_read_b128 v[0:3], v1 offset:528
	ds_read_b128 v[24:27], v16 offset:512
	ds_read_b128 v[16:19], v16 offset:528
	v_and_b32_e32 v32, 15, v168
	v_ashrrev_i32_e32 v33, 2, v168
	v_and_or_b32 v37, v33, s36, v32
	s_lshl_b32 s42, s76, 8
	v_add_u32_e32 v38, s42, v37
	v_cmp_le_i32_e32 vcc, s69, v38
	s_and_saveexec_b64 s[36:37], vcc
	s_xor_b64 s[36:37], exec, s[36:37]
	v_add_u32_e32 v39, 0x40000, v37
	s_andn2_saveexec_b64 s[36:37], s[36:37]
	v_lshl_add_u32 v32, v37, 2, 0
	v_add_u32_e32 v32, 0x20900, v32
	ds_read_b32 v39, v32
	s_or_b64 exec, exec, s[36:37]
	v_lshl_add_u32 v36, v37, 2, s88
	ds_read_b32 v209, v36 offset:2048
	v_or_b32_e32 v208, 16, v37
	v_add_u32_e32 v32, s42, v208
	v_cmp_le_i32_e32 vcc, s69, v32
	s_and_saveexec_b64 s[36:37], vcc
	s_xor_b64 s[36:37], exec, s[36:37]
	v_add_u32_e32 v207, 0x40010, v37
	s_andn2_saveexec_b64 s[36:37], s[36:37]
	v_lshl_add_u32 v32, v208, 2, 0
	v_add_u32_e32 v32, 0x20900, v32
	ds_read_b32 v207, v32
	s_or_b64 exec, exec, s[36:37]
	s_mov_b32 s36, 0x39929cec
	s_waitcnt lgkmcnt(6)
	v_pk_mul_f32 v[32:33], v[30:31], s[36:37] op_sel_hi:[1,0]
	v_pk_mul_f32 v[34:35], v[28:29], s[36:37] op_sel_hi:[1,0]
	s_waitcnt lgkmcnt(5)
	v_pk_mul_f32 v[28:29], v[22:23], s[36:37] op_sel_hi:[1,0]
	v_pk_mul_f32 v[30:31], v[20:21], s[36:37] op_sel_hi:[1,0]
	s_waitcnt lgkmcnt(2)
	v_pk_mul_f32 v[20:21], v[26:27], s[36:37] op_sel_hi:[1,0]
	v_pk_mul_f32 v[22:23], v[24:25], s[36:37] op_sel_hi:[1,0]
	s_waitcnt lgkmcnt(0)
	v_mul_f32_e32 v26, 0x41800000, v209
	v_pk_fma_f32 v[24:25], v[154:155], v[32:33], v[14:15]
	v_pk_fma_f32 v[152:153], v[152:153], v[34:35], v[12:13]
	v_pk_mul_f32 v[154:155], v[24:25], v[26:27] op_sel_hi:[1,0]
	v_pk_mul_f32 v[24:25], v[152:153], v[26:27] op_sel_hi:[1,0]
	v_pk_fma_f32 v[152:153], v[158:159], v[28:29], v[10:11]
	v_pk_fma_f32 v[156:157], v[156:157], v[30:31], v[8:9]
	v_pk_mul_f32 v[152:153], v[152:153], v[26:27] op_sel_hi:[1,0]
	v_pk_mul_f32 v[156:157], v[156:157], v[26:27] op_sel_hi:[1,0]
	v_med3_f32 v27, v24, s9, v200
	v_med3_f32 v25, v25, s9, v200
	v_mov_b32_e32 v24, v169
	v_med3_f32 v156, v156, s9, v200
	v_med3_f32 v157, v157, s9, v200
	v_cvt_pk_fp8_f32 v24, v27, v25
	v_mov_b32_e32 v25, v169
	v_cvt_pk_fp8_f32 v25, v156, v157
	v_med3_f32 v154, v154, s9, v200
	v_med3_f32 v152, v152, s9, v200
	v_med3_f32 v27, v155, s9, v200
	v_med3_f32 v153, v153, s9, v200
	v_pk_mul_f32 v[18:19], v[18:19], s[36:37] op_sel_hi:[1,0]
	v_pk_mul_f32 v[16:17], v[16:17], s[36:37] op_sel_hi:[1,0]
	v_cvt_pk_fp8_f32 v24, v154, v27 op_sel:[0,0,1]
	v_cvt_pk_fp8_f32 v25, v152, v153 op_sel:[0,0,1]
	v_pk_fma_f32 v[152:153], v[162:163], v[20:21], v[6:7]
	v_pk_fma_f32 v[154:155], v[160:161], v[22:23], v[4:5]
	v_pk_mul_f32 v[156:157], v[152:153], v[26:27] op_sel_hi:[1,0]
	v_pk_mul_f32 v[152:153], v[154:155], v[26:27] op_sel_hi:[1,0]
	v_pk_fma_f32 v[154:155], v[166:167], v[18:19], v[2:3]
	v_pk_fma_f32 v[158:159], v[164:165], v[16:17], v[0:1]
	v_pk_mul_f32 v[154:155], v[154:155], v[26:27] op_sel_hi:[1,0]
	v_pk_mul_f32 v[26:27], v[158:159], v[26:27] op_sel_hi:[1,0]
	v_med3_f32 v158, v152, s9, v200
	v_med3_f32 v153, v153, s9, v200
	v_mov_b32_e32 v152, v169
	v_cvt_pk_fp8_f32 v152, v158, v153
	v_med3_f32 v26, v26, s9, v200
	v_med3_f32 v27, v27, s9, v200
	v_mov_b32_e32 v153, v169
	v_med3_f32 v156, v156, s9, v200
	v_cvt_pk_fp8_f32 v153, v26, v27
	v_med3_f32 v26, v157, s9, v200
	v_cvt_pk_fp8_f32 v152, v156, v26 op_sel:[0,0,1]
	v_lshl_add_u32 v26, v208, 2, s88
	ds_read_b32 v26, v26 offset:2048
	v_lshrrev_b32_e32 v210, 1, v168
	v_med3_f32 v154, v154, s9, v200
	v_med3_f32 v27, v155, s9, v200
	s_lshl_b32 s36, s75, 8
	v_cvt_pk_fp8_f32 v153, v154, v27 op_sel:[0,0,1]
	s_and_b32 s36, s36, 0x300
	v_and_b32_e32 v27, 0x70, v210
	v_and_b32_e32 v156, 16, v168
	v_or_b32_e32 v168, s36, v27
	s_waitcnt lgkmcnt(0)
; #define GAS __attribute__((address_space(1)))
;     __device__ __forceinline__ void operator()(const f32x4 (&acc)[2][2][4][2], const Unit& u, int wr, int wc, int fr, int fq, PG8_LAS unsigned* scr) const {
;     ...
;             for (int mp = 0; mp < 4; mp += 2) { unsigned wq[2][2][2]; int dsts[2];
; #pragma unroll
;                 for (int hm = 0; hm < 2; ++hm) { const int m = mp + hm; const int r = ai * HALF + wr * 64 + m * 16 + fr; const int pos = u.rb * 256 + r;
;                     dsts[hm] = pos < u.cnt ? (int)scr[r] : trash + r; const float rg = __uint_as_float(scr[512 + r]) * 16.0f;
; #pragma unroll
;                     for (int bj = 0; bj < 2; ++bj) { f32x4 v0 = (acc[ai][bj][m][0] * cs[bj][0] + bv[bj][0]) * rg, v1 = (acc[ai][bj][m][1] * cs[bj][1] + bv[bj][1]) * rg;
; #pragma unroll
;                         for (int q = 0; q < 4; ++q) { v0[q] = fminf(fmaxf(v0[q], -448.0f), 448.0f); v1[q] = fminf(fmaxf(v1[q], -448.0f), 448.0f); }
;                         int w0 = __builtin_amdgcn_cvt_pk_fp8_f32(v0[0], v0[1], 0, false); w0 = __builtin_amdgcn_cvt_pk_fp8_f32(v0[2], v0[3], w0, true);
;                         int w1 = __builtin_amdgcn_cvt_pk_fp8_f32(v1[0], v1[1], 0, false); w1 = __builtin_amdgcn_cvt_pk_fp8_f32(v1[2], v1[3], w1, true);
;                         wq[hm][bj][0] = (unsigned)w0; wq[hm][bj][1] = (unsigned)w1; } }
;                 const int odd = fq & 1; unsigned char* rowp = (unsigned char*)y4 + (size_t)(odd ? dsts[1] : dsts[0]) * 1024 + (c0 - 8 * odd);
; #pragma unroll
;                 for (int bj = 0; bj < 2; ++bj) {
;                     auto r0 = __builtin_amdgcn_permlane16_swap(wq[0][bj][0], wq[1][bj][0], false, false); auto r1 = __builtin_amdgcn_permlane16_swap(wq[0][bj][1], wq[1][bj][1], false, false);
;                     *(GAS u32x4*)(rowp + bj * HALF) = (u32x4){(unsigned)r0[0], (unsigned)r1[0], (unsigned)r0[1], (unsigned)r1[1]}; } }
	v_mul_f32_e32 v154, 0x41800000, v26
	v_pk_fma_f32 v[26:27], v[142:143], v[32:33], v[14:15]
	v_pk_fma_f32 v[140:141], v[140:141], v[34:35], v[12:13]
	v_pk_mul_f32 v[142:143], v[26:27], v[154:155] op_sel_hi:[1,0]
	v_pk_mul_f32 v[26:27], v[140:141], v[154:155] op_sel_hi:[1,0]
	v_pk_fma_f32 v[136:137], v[136:137], v[30:31], v[8:9]
	v_med3_f32 v140, v26, s9, v200
	v_pk_mul_f32 v[136:137], v[136:137], v[154:155] op_sel_hi:[1,0]
	v_med3_f32 v27, v27, s9, v200
	v_mov_b32_e32 v26, v169
	v_med3_f32 v136, v136, s9, v200
	v_med3_f32 v137, v137, s9, v200
	v_cvt_pk_fp8_f32 v26, v140, v27
	v_mov_b32_e32 v27, v169
	v_cvt_pk_fp8_f32 v27, v136, v137
	v_pk_fma_f32 v[138:139], v[138:139], v[28:29], v[10:11]
	v_med3_f32 v141, v142, s9, v200
	v_pk_mul_f32 v[138:139], v[138:139], v[154:155] op_sel_hi:[1,0]
	v_med3_f32 v136, v143, s9, v200
	v_med3_f32 v138, v138, s9, v200
	v_med3_f32 v137, v139, s9, v200
	v_cvt_pk_fp8_f32 v27, v138, v137 op_sel:[0,0,1]
	v_pk_fma_f32 v[138:139], v[148:149], v[22:23], v[4:5]
	v_cvt_pk_fp8_f32 v26, v141, v136 op_sel:[0,0,1]
	v_pk_fma_f32 v[136:137], v[150:151], v[20:21], v[6:7]
	v_pk_mul_f32 v[138:139], v[138:139], v[154:155] op_sel_hi:[1,0]
	v_pk_fma_f32 v[140:141], v[146:147], v[18:19], v[2:3]
	v_pk_fma_f32 v[142:143], v[144:145], v[16:17], v[0:1]
	v_pk_mul_f32 v[136:137], v[136:137], v[154:155] op_sel_hi:[1,0]
	v_pk_mul_f32 v[140:141], v[140:141], v[154:155] op_sel_hi:[1,0]
	v_pk_mul_f32 v[142:143], v[142:143], v[154:155] op_sel_hi:[1,0]
	v_med3_f32 v138, v138, s9, v200
	v_med3_f32 v139, v139, s9, v200
	v_mov_b32_e32 v154, v169
	v_cvt_pk_fp8_f32 v154, v138, v139
	v_med3_f32 v142, v142, s9, v200
	v_med3_f32 v143, v143, s9, v200
	v_mov_b32_e32 v155, v169
	v_med3_f32 v136, v136, s9, v200
	v_cvt_pk_fp8_f32 v155, v142, v143
	v_med3_f32 v137, v137, s9, v200
	v_cmp_eq_u32_e32 vcc, 0, v156
	v_cvt_pk_fp8_f32 v154, v136, v137 op_sel:[0,0,1]
	v_med3_f32 v140, v140, s9, v200
	v_cndmask_b32_e32 v136, v207, v39, vcc
	v_ashrrev_i32_e32 v137, 31, v136
	v_med3_f32 v138, v141, s9, v200
	v_lshlrev_b64 v[136:137], 10, v[136:137]
	v_cvt_pk_fp8_f32 v155, v140, v138 op_sel:[0,0,1]
	v_lshl_add_u64 v[136:137], s[30:31], 0, v[136:137]
	v_lshl_add_u64 v[136:137], v[136:137], 0, v[168:169]
	v_permlane16_swap_b32_e32 v24, v26
	v_permlane16_swap_b32_e32 v25, v27
	global_store_dwordx4 v[136:137], v[24:27], off
	v_permlane16_swap_b32_e32 v152, v154
	s_nop 0
	v_or_b32_e32 v25, 32, v37
	v_add_u32_e32 v24, s42, v25
	v_permlane16_swap_b32_e32 v153, v155
	v_cmp_le_i32_e64 s[36:37], s69, v24
	global_store_dwordx4 v[136:137], v[152:155], off offset:128
	s_and_b64 s[98:99], exec, s[44:45]
	s_cbranch_scc0 .Lp6_epi_nobar
	s_barrier
.Lp6_epi_nobar:
	s_and_saveexec_b64 s[76:77], s[36:37]
	s_xor_b64 s[36:37], exec, s[76:77]
	v_add_u32_e32 v24, 0x40020, v37
	s_andn2_saveexec_b64 s[36:37], s[36:37]
	v_lshl_add_u32 v24, v25, 2, 0
	v_add_u32_e32 v24, 0x20900, v24
	ds_read_b32 v24, v24
	s_or_b64 exec, exec, s[36:37]
	v_lshl_add_u32 v25, v25, 2, s88
	ds_read_b32 v27, v25 offset:2048
	v_or_b32_e32 v26, 48, v37
	v_add_u32_e32 v25, s42, v26
	v_cmp_le_i32_e64 s[36:37], s69, v25
	s_and_saveexec_b64 s[42:43], s[36:37]
	s_xor_b64 s[36:37], exec, s[42:43]
	v_add_u32_e32 v25, 0x40030, v37
	s_andn2_saveexec_b64 s[36:37], s[36:37]
	v_lshl_add_u32 v25, v26, 2, 0
	v_add_u32_e32 v25, 0x20900, v25
	ds_read_b32 v25, v25
	s_or_b64 exec, exec, s[36:37]
	s_waitcnt lgkmcnt(0)
	v_mul_f32_e32 v136, 0x41800000, v27
	v_pk_fma_f32 v[132:133], v[132:133], v[34:35], v[12:13]
	v_pk_fma_f32 v[124:125], v[124:125], v[30:31], v[8:9]
	v_pk_mul_f32 v[132:133], v[132:133], v[136:137] op_sel_hi:[1,0]
	v_pk_mul_f32 v[124:125], v[124:125], v[136:137] op_sel_hi:[1,0]
	v_med3_f32 v27, v132, s9, v200
	v_med3_f32 v39, v124, s9, v200
	v_med3_f32 v132, v133, s9, v200
	v_med3_f32 v133, v125, s9, v200
	v_mov_b32_e32 v124, v169
	v_mov_b32_e32 v125, v169
	v_cvt_pk_fp8_f32 v124, v27, v132
	v_cvt_pk_fp8_f32 v125, v39, v133
	v_pk_fma_f32 v[134:135], v[134:135], v[32:33], v[14:15]
	v_pk_fma_f32 v[126:127], v[126:127], v[28:29], v[10:11]
	v_lshl_add_u32 v26, v26, 2, s88
	v_pk_mul_f32 v[134:135], v[134:135], v[136:137] op_sel_hi:[1,0]
	v_pk_mul_f32 v[126:127], v[126:127], v[136:137] op_sel_hi:[1,0]
	v_pk_fma_f32 v[128:129], v[128:129], v[22:23], v[4:5]
	v_pk_fma_f32 v[120:121], v[120:121], v[16:17], v[0:1]
	ds_read_b32 v26, v26 offset:2048
	v_med3_f32 v134, v134, s9, v200
	v_med3_f32 v126, v126, s9, v200
	v_med3_f32 v27, v135, s9, v200
	v_med3_f32 v39, v127, s9, v200
	v_pk_mul_f32 v[128:129], v[128:129], v[136:137] op_sel_hi:[1,0]
	v_pk_mul_f32 v[120:121], v[120:121], v[136:137] op_sel_hi:[1,0]
	v_cvt_pk_fp8_f32 v124, v134, v27 op_sel:[0,0,1]
	v_cvt_pk_fp8_f32 v125, v126, v39 op_sel:[0,0,1]
	v_med3_f32 v27, v128, s9, v200
	v_med3_f32 v39, v120, s9, v200
	v_med3_f32 v128, v129, s9, v200
	v_med3_f32 v129, v121, s9, v200
	v_mov_b32_e32 v121, v169
	v_pk_fma_f32 v[126:127], v[130:131], v[20:21], v[6:7]
	v_mov_b32_e32 v120, v169
	v_cvt_pk_fp8_f32 v121, v39, v129
	v_pk_mul_f32 v[126:127], v[126:127], v[136:137] op_sel_hi:[1,0]
	v_pk_fma_f32 v[122:123], v[122:123], v[18:19], v[2:3]
	v_cvt_pk_fp8_f32 v120, v27, v128
	v_pk_mul_f32 v[122:123], v[122:123], v[136:137] op_sel_hi:[1,0]
	v_med3_f32 v27, v127, s9, v200
	s_waitcnt lgkmcnt(0)
; #define GAS __attribute__((address_space(1)))
;     __device__ __forceinline__ void operator()(const f32x4 (&acc)[2][2][4][2], const Unit& u, int wr, int wc, int fr, int fq, PG8_LAS unsigned* scr) const {
;     ...
;             for (int mp = 0; mp < 4; mp += 2) { unsigned wq[2][2][2]; int dsts[2];
; #pragma unroll
;                 for (int hm = 0; hm < 2; ++hm) { const int m = mp + hm; const int r = ai * HALF + wr * 64 + m * 16 + fr; const int pos = u.rb * 256 + r;
;                     dsts[hm] = pos < u.cnt ? (int)scr[r] : trash + r; const float rg = __uint_as_float(scr[512 + r]) * 16.0f;
; #pragma unroll
;                     for (int bj = 0; bj < 2; ++bj) { f32x4 v0 = (acc[ai][bj][m][0] * cs[bj][0] + bv[bj][0]) * rg, v1 = (acc[ai][bj][m][1] * cs[bj][1] + bv[bj][1]) * rg;
; #pragma unroll
;                         for (int q = 0; q < 4; ++q) { v0[q] = fminf(fmaxf(v0[q], -448.0f), 448.0f); v1[q] = fminf(fmaxf(v1[q], -448.0f), 448.0f); }
;                         int w0 = __builtin_amdgcn_cvt_pk_fp8_f32(v0[0], v0[1], 0, false); w0 = __builtin_amdgcn_cvt_pk_fp8_f32(v0[2], v0[3], w0, true);
;                         int w1 = __builtin_amdgcn_cvt_pk_fp8_f32(v1[0], v1[1], 0, false); w1 = __builtin_amdgcn_cvt_pk_fp8_f32(v1[2], v1[3], w1, true);
;                         wq[hm][bj][0] = (unsigned)w0; wq[hm][bj][1] = (unsigned)w1; } }
;                 const int odd = fq & 1; unsigned char* rowp = (unsigned char*)y4 + (size_t)(odd ? dsts[1] : dsts[0]) * 1024 + (c0 - 8 * odd);
; #pragma unroll
;                 for (int bj = 0; bj < 2; ++bj) {
;                     auto r0 = __builtin_amdgcn_permlane16_swap(wq[0][bj][0], wq[1][bj][0], false, false); auto r1 = __builtin_amdgcn_permlane16_swap(wq[0][bj][1], wq[1][bj][1], false, false);
;                     *(GAS u32x4*)(rowp + bj * HALF) = (u32x4){(unsigned)r0[0], (unsigned)r1[0], (unsigned)r0[1], (unsigned)r1[1]}; } }
	v_mul_f32_e32 v26, 0x41800000, v26
	v_pk_fma_f32 v[108:109], v[108:109], v[30:31], v[8:9]
	v_med3_f32 v122, v122, s9, v200
	v_med3_f32 v39, v123, s9, v200
	v_pk_fma_f32 v[116:117], v[116:117], v[34:35], v[12:13]
	v_pk_mul_f32 v[108:109], v[108:109], v[26:27] op_sel_hi:[1,0]
	v_med3_f32 v126, v126, s9, v200
	v_cvt_pk_fp8_f32 v121, v122, v39 op_sel:[0,0,1]
	v_pk_fma_f32 v[118:119], v[118:119], v[32:33], v[14:15]
	v_pk_mul_f32 v[116:117], v[116:117], v[26:27] op_sel_hi:[1,0]
	v_pk_fma_f32 v[110:111], v[110:111], v[28:29], v[10:11]
	v_med3_f32 v39, v108, s9, v200
	v_med3_f32 v109, v109, s9, v200
	v_mov_b32_e32 v127, v169
	v_cvt_pk_fp8_f32 v120, v126, v27 op_sel:[0,0,1]
	v_pk_mul_f32 v[118:119], v[118:119], v[26:27] op_sel_hi:[1,0]
	v_pk_mul_f32 v[110:111], v[110:111], v[26:27] op_sel_hi:[1,0]
	v_med3_f32 v27, v116, s9, v200
	v_med3_f32 v108, v117, s9, v200
	v_mov_b32_e32 v126, v169
	v_cvt_pk_fp8_f32 v127, v39, v109
	v_cvt_pk_fp8_f32 v126, v27, v108
	v_med3_f32 v110, v110, s9, v200
	v_med3_f32 v39, v111, s9, v200
	v_med3_f32 v116, v118, s9, v200
	v_med3_f32 v27, v119, s9, v200
	v_cvt_pk_fp8_f32 v127, v110, v39 op_sel:[0,0,1]
	v_pk_fma_f32 v[108:109], v[114:115], v[20:21], v[6:7]
	v_pk_fma_f32 v[110:111], v[112:113], v[22:23], v[4:5]
	v_pk_fma_f32 v[106:107], v[106:107], v[18:19], v[2:3]
	v_pk_fma_f32 v[104:105], v[104:105], v[16:17], v[0:1]
	v_cvt_pk_fp8_f32 v126, v116, v27 op_sel:[0,0,1]
	v_pk_mul_f32 v[108:109], v[108:109], v[26:27] op_sel_hi:[1,0]
	v_pk_mul_f32 v[110:111], v[110:111], v[26:27] op_sel_hi:[1,0]
	v_pk_mul_f32 v[106:107], v[106:107], v[26:27] op_sel_hi:[1,0]
	v_pk_mul_f32 v[26:27], v[104:105], v[26:27] op_sel_hi:[1,0]
	v_med3_f32 v39, v110, s9, v200
	v_med3_f32 v26, v26, s9, v200
	v_med3_f32 v104, v111, s9, v200
	v_med3_f32 v27, v27, s9, v200
	v_mov_b32_e32 v122, v169
	v_mov_b32_e32 v123, v169
	v_cvt_pk_fp8_f32 v122, v39, v104
	v_cvt_pk_fp8_f32 v123, v26, v27
	v_med3_f32 v105, v108, s9, v200
	v_med3_f32 v106, v106, s9, v200
	v_med3_f32 v26, v109, s9, v200
	v_med3_f32 v27, v107, s9, v200
	v_cvt_pk_fp8_f32 v122, v105, v26 op_sel:[0,0,1]
	v_cvt_pk_fp8_f32 v123, v106, v27 op_sel:[0,0,1]
	v_cndmask_b32_e32 v24, v25, v24, vcc
	v_ashrrev_i32_e32 v25, 31, v24
	v_lshlrev_b64 v[24:25], 10, v[24:25]
	v_lshl_add_u64 v[24:25], s[30:31], 0, v[24:25]
	v_lshl_add_u64 v[24:25], v[24:25], 0, v[168:169]
	v_permlane16_swap_b32_e32 v124, v126
	v_permlane16_swap_b32_e32 v125, v127
	v_permlane16_swap_b32_e32 v120, v122
	v_permlane16_swap_b32_e32 v121, v123
	global_store_dwordx4 v[24:25], v[124:127], off
	global_store_dwordx4 v[24:25], v[120:123], off offset:128
	v_add_u32_e32 v24, 0x80, v38
	v_cmp_le_i32_e64 s[36:37], s69, v24
	s_and_saveexec_b64 s[42:43], s[36:37]
	s_xor_b64 s[36:37], exec, s[42:43]
	v_add_u32_e32 v24, 0x40080, v37
	s_andn2_saveexec_b64 s[36:37], s[36:37]
	ds_read_b32 v24, v36 offset:512
	s_or_b64 exec, exec, s[36:37]
	ds_read_b32 v26, v36 offset:2560
	v_add_u32_e32 v25, 0x90, v38
	v_cmp_le_i32_e64 s[36:37], s69, v25
	s_and_saveexec_b64 s[42:43], s[36:37]
	s_xor_b64 s[36:37], exec, s[42:43]
	v_add_u32_e32 v25, 0x40090, v37
	s_andn2_saveexec_b64 s[36:37], s[36:37]
	ds_read_b32 v25, v36 offset:576
	s_or_b64 exec, exec, s[36:37]
	s_waitcnt lgkmcnt(0)
	v_mul_f32_e32 v26, 0x41800000, v26
	v_pk_fma_f32 v[96:97], v[96:97], v[34:35], v[12:13]
	v_pk_fma_f32 v[88:89], v[88:89], v[30:31], v[8:9]
	v_pk_fma_f32 v[98:99], v[98:99], v[32:33], v[14:15]
	v_pk_mul_f32 v[96:97], v[96:97], v[26:27] op_sel_hi:[1,0]
	v_pk_fma_f32 v[90:91], v[90:91], v[28:29], v[10:11]
	v_pk_mul_f32 v[88:89], v[88:89], v[26:27] op_sel_hi:[1,0]
	v_pk_mul_f32 v[98:99], v[98:99], v[26:27] op_sel_hi:[1,0]
	v_pk_mul_f32 v[90:91], v[90:91], v[26:27] op_sel_hi:[1,0]
	v_med3_f32 v27, v96, s9, v200
	v_med3_f32 v39, v88, s9, v200
	v_med3_f32 v96, v97, s9, v200
	v_med3_f32 v97, v89, s9, v200
	v_mov_b32_e32 v89, v169
	v_mov_b32_e32 v88, v169
	v_cvt_pk_fp8_f32 v89, v39, v97
	v_cvt_pk_fp8_f32 v88, v27, v96
	v_med3_f32 v90, v90, s9, v200
	v_med3_f32 v27, v99, s9, v200
	v_med3_f32 v39, v91, s9, v200
	v_pk_fma_f32 v[96:97], v[100:101], v[22:23], v[4:5]
	v_med3_f32 v98, v98, s9, v200
	v_cvt_pk_fp8_f32 v89, v90, v39 op_sel:[0,0,1]
	v_pk_fma_f32 v[90:91], v[102:103], v[20:21], v[6:7]
	v_pk_mul_f32 v[96:97], v[96:97], v[26:27] op_sel_hi:[1,0]
	v_pk_fma_f32 v[94:95], v[94:95], v[18:19], v[2:3]
	v_pk_fma_f32 v[92:93], v[92:93], v[16:17], v[0:1]
	v_cvt_pk_fp8_f32 v88, v98, v27 op_sel:[0,0,1]
	v_pk_mul_f32 v[90:91], v[90:91], v[26:27] op_sel_hi:[1,0]
	v_pk_mul_f32 v[94:95], v[94:95], v[26:27] op_sel_hi:[1,0]
	v_pk_mul_f32 v[26:27], v[92:93], v[26:27] op_sel_hi:[1,0]
	v_med3_f32 v39, v96, s9, v200
	v_med3_f32 v93, v97, s9, v200
	v_mov_b32_e32 v92, v169
	v_med3_f32 v26, v26, s9, v200
	v_med3_f32 v27, v27, s9, v200
	v_cvt_pk_fp8_f32 v92, v39, v93
	v_mov_b32_e32 v93, v169
	v_cvt_pk_fp8_f32 v93, v26, v27
	ds_read_b32 v26, v36 offset:2624
	v_med3_f32 v27, v91, s9, v200
	v_pk_fma_f32 v[84:85], v[84:85], v[34:35], v[12:13]
	v_pk_fma_f32 v[80:81], v[80:81], v[30:31], v[8:9]
	v_med3_f32 v90, v90, s9, v200
	s_waitcnt lgkmcnt(0)
; #define GAS __attribute__((address_space(1)))
;     __device__ __forceinline__ void operator()(const f32x4 (&acc)[2][2][4][2], const Unit& u, int wr, int wc, int fr, int fq, PG8_LAS unsigned* scr) const {
;     ...
;             for (int mp = 0; mp < 4; mp += 2) { unsigned wq[2][2][2]; int dsts[2];
; #pragma unroll
;                 for (int hm = 0; hm < 2; ++hm) { const int m = mp + hm; const int r = ai * HALF + wr * 64 + m * 16 + fr; const int pos = u.rb * 256 + r;
;                     dsts[hm] = pos < u.cnt ? (int)scr[r] : trash + r; const float rg = __uint_as_float(scr[512 + r]) * 16.0f;
; #pragma unroll
;                     for (int bj = 0; bj < 2; ++bj) { f32x4 v0 = (acc[ai][bj][m][0] * cs[bj][0] + bv[bj][0]) * rg, v1 = (acc[ai][bj][m][1] * cs[bj][1] + bv[bj][1]) * rg;
; #pragma unroll
;                         for (int q = 0; q < 4; ++q) { v0[q] = fminf(fmaxf(v0[q], -448.0f), 448.0f); v1[q] = fminf(fmaxf(v1[q], -448.0f), 448.0f); }
;                         int w0 = __builtin_amdgcn_cvt_pk_fp8_f32(v0[0], v0[1], 0, false); w0 = __builtin_amdgcn_cvt_pk_fp8_f32(v0[2], v0[3], w0, true);
;                         int w1 = __builtin_amdgcn_cvt_pk_fp8_f32(v1[0], v1[1], 0, false); w1 = __builtin_amdgcn_cvt_pk_fp8_f32(v1[2], v1[3], w1, true);
;                         wq[hm][bj][0] = (unsigned)w0; wq[hm][bj][1] = (unsigned)w1; } }
;                 const int odd = fq & 1; unsigned char* rowp = (unsigned char*)y4 + (size_t)(odd ? dsts[1] : dsts[0]) * 1024 + (c0 - 8 * odd);
; #pragma unroll
;                 for (int bj = 0; bj < 2; ++bj) {
;                     auto r0 = __builtin_amdgcn_permlane16_swap(wq[0][bj][0], wq[1][bj][0], false, false); auto r1 = __builtin_amdgcn_permlane16_swap(wq[0][bj][1], wq[1][bj][1], false, false);
;                     *(GAS u32x4*)(rowp + bj * HALF) = (u32x4){(unsigned)r0[0], (unsigned)r1[0], (unsigned)r0[1], (unsigned)r1[1]}; } }
	v_mul_f32_e32 v26, 0x41800000, v26
	v_med3_f32 v94, v94, s9, v200
	v_med3_f32 v39, v95, s9, v200
	v_pk_fma_f32 v[86:87], v[86:87], v[32:33], v[14:15]
	v_pk_mul_f32 v[84:85], v[84:85], v[26:27] op_sel_hi:[1,0]
	v_pk_fma_f32 v[82:83], v[82:83], v[28:29], v[10:11]
	v_pk_mul_f32 v[80:81], v[80:81], v[26:27] op_sel_hi:[1,0]
	v_cvt_pk_fp8_f32 v92, v90, v27 op_sel:[0,0,1]
	v_cvt_pk_fp8_f32 v93, v94, v39 op_sel:[0,0,1]
	v_pk_mul_f32 v[86:87], v[86:87], v[26:27] op_sel_hi:[1,0]
	v_pk_mul_f32 v[82:83], v[82:83], v[26:27] op_sel_hi:[1,0]
	v_med3_f32 v27, v84, s9, v200
	v_med3_f32 v39, v80, s9, v200
	v_med3_f32 v80, v85, s9, v200
	v_mov_b32_e32 v90, v169
	v_med3_f32 v81, v81, s9, v200
	v_cvt_pk_fp8_f32 v90, v27, v80
	v_mov_b32_e32 v91, v169
	v_cvt_pk_fp8_f32 v91, v39, v81
	v_med3_f32 v84, v86, s9, v200
	v_med3_f32 v27, v87, s9, v200
	v_pk_fma_f32 v[62:63], v[62:63], v[20:21], v[6:7]
	v_pk_fma_f32 v[60:61], v[60:61], v[22:23], v[4:5]
	v_pk_fma_f32 v[58:59], v[58:59], v[18:19], v[2:3]
	v_pk_fma_f32 v[56:57], v[56:57], v[16:17], v[0:1]
	v_med3_f32 v82, v82, s9, v200
	v_med3_f32 v39, v83, s9, v200
	v_cvt_pk_fp8_f32 v90, v84, v27 op_sel:[0,0,1]
	v_pk_mul_f32 v[62:63], v[62:63], v[26:27] op_sel_hi:[1,0]
	v_pk_mul_f32 v[60:61], v[60:61], v[26:27] op_sel_hi:[1,0]
	v_pk_mul_f32 v[58:59], v[58:59], v[26:27] op_sel_hi:[1,0]
	v_pk_mul_f32 v[26:27], v[56:57], v[26:27] op_sel_hi:[1,0]
	v_cvt_pk_fp8_f32 v91, v82, v39 op_sel:[0,0,1]
	v_med3_f32 v39, v60, s9, v200
	v_med3_f32 v26, v26, s9, v200
	v_med3_f32 v56, v61, s9, v200
	v_med3_f32 v27, v27, s9, v200
	v_mov_b32_e32 v94, v169
	v_mov_b32_e32 v95, v169
	v_cvt_pk_fp8_f32 v94, v39, v56
	v_cvt_pk_fp8_f32 v95, v26, v27
	v_med3_f32 v57, v62, s9, v200
	v_med3_f32 v58, v58, s9, v200
	v_med3_f32 v26, v63, s9, v200
	v_med3_f32 v27, v59, s9, v200
	v_cvt_pk_fp8_f32 v94, v57, v26 op_sel:[0,0,1]
	v_cvt_pk_fp8_f32 v95, v58, v27 op_sel:[0,0,1]
	v_cndmask_b32_e32 v24, v25, v24, vcc
	v_ashrrev_i32_e32 v25, 31, v24
	v_lshlrev_b64 v[24:25], 10, v[24:25]
	v_lshl_add_u64 v[24:25], s[30:31], 0, v[24:25]
	v_lshl_add_u64 v[24:25], v[24:25], 0, v[168:169]
	v_permlane16_swap_b32_e32 v88, v90
	v_permlane16_swap_b32_e32 v89, v91
	v_permlane16_swap_b32_e32 v92, v94
	v_permlane16_swap_b32_e32 v93, v95
	global_store_dwordx4 v[24:25], v[88:91], off
	global_store_dwordx4 v[24:25], v[92:95], off offset:128
	v_add_u32_e32 v24, 0xa0, v38
	v_cmp_le_i32_e64 s[36:37], s69, v24
	s_and_saveexec_b64 s[42:43], s[36:37]
	s_xor_b64 s[36:37], exec, s[42:43]
	v_add_u32_e32 v24, 0x400a0, v37
	s_andn2_saveexec_b64 s[36:37], s[36:37]
	ds_read_b32 v24, v36 offset:640
	s_or_b64 exec, exec, s[36:37]
	ds_read_b32 v26, v36 offset:2688
	v_add_u32_e32 v25, 0xb0, v38
	v_cmp_le_i32_e64 s[36:37], s69, v25
	s_and_saveexec_b64 s[42:43], s[36:37]
	s_xor_b64 s[36:37], exec, s[42:43]
	v_add_u32_e32 v25, 0x400b0, v37
	s_andn2_saveexec_b64 s[36:37], s[36:37]
	ds_read_b32 v25, v36 offset:704
	s_or_b64 exec, exec, s[36:37]
	s_waitcnt lgkmcnt(0)
; #define GAS __attribute__((address_space(1)))
; #define PG8_BAR __builtin_amdgcn_s_barrier()
;     __device__ __forceinline__ void operator()(const f32x4 (&acc)[2][2][4][2], const Unit& u, int wr, int wc, int fr, int fq, PG8_LAS unsigned* scr) const {
;     ...
;             for (int mp = 0; mp < 4; mp += 2) { unsigned wq[2][2][2]; int dsts[2];
; #pragma unroll
;                 for (int hm = 0; hm < 2; ++hm) { const int m = mp + hm; const int r = ai * HALF + wr * 64 + m * 16 + fr; const int pos = u.rb * 256 + r;
;                     dsts[hm] = pos < u.cnt ? (int)scr[r] : trash + r; const float rg = __uint_as_float(scr[512 + r]) * 16.0f;
; #pragma unroll
;                     for (int bj = 0; bj < 2; ++bj) { f32x4 v0 = (acc[ai][bj][m][0] * cs[bj][0] + bv[bj][0]) * rg, v1 = (acc[ai][bj][m][1] * cs[bj][1] + bv[bj][1]) * rg;
; #pragma unroll
;                         for (int q = 0; q < 4; ++q) { v0[q] = fminf(fmaxf(v0[q], -448.0f), 448.0f); v1[q] = fminf(fmaxf(v1[q], -448.0f), 448.0f); }
;                         int w0 = __builtin_amdgcn_cvt_pk_fp8_f32(v0[0], v0[1], 0, false); w0 = __builtin_amdgcn_cvt_pk_fp8_f32(v0[2], v0[3], w0, true);
;                         int w1 = __builtin_amdgcn_cvt_pk_fp8_f32(v1[0], v1[1], 0, false); w1 = __builtin_amdgcn_cvt_pk_fp8_f32(v1[2], v1[3], w1, true);
;                         wq[hm][bj][0] = (unsigned)w0; wq[hm][bj][1] = (unsigned)w1; } }
;                 const int odd = fq & 1; unsigned char* rowp = (unsigned char*)y4 + (size_t)(odd ? dsts[1] : dsts[0]) * 1024 + (c0 - 8 * odd);
; #pragma unroll
;                 for (int bj = 0; bj < 2; ++bj) {
;                     auto r0 = __builtin_amdgcn_permlane16_swap(wq[0][bj][0], wq[1][bj][0], false, false); auto r1 = __builtin_amdgcn_permlane16_swap(wq[0][bj][1], wq[1][bj][1], false, false);
;                     *(GAS u32x4*)(rowp + bj * HALF) = (u32x4){(unsigned)r0[0], (unsigned)r1[0], (unsigned)r0[1], (unsigned)r1[1]}; } }
; template <class Epi, class Sched, bool GATHER, int MODE>
; __device__ __forceinline__ void gemm_phase(PG8_LAS unsigned char* lds, PG8_LAS unsigned* scr, const Gemm g, const Sched& S, const Epi& E, int tid_in) {
;     ...
;         if (!has_next) break;
;         cur = nxt; cA = nA; cB = nB; ++ui;
;         if (GATHER) { const u32x4 nx = gather_read(cur); c0[0] = nx[0]; c0[1] = nx[1]; c1[0] = nx[2]; c1[1] = nx[3]; }
;         if (wr == 1) PG8_BAR;
	v_mul_f32_e32 v38, 0x41800000, v26
	v_pk_fma_f32 v[26:27], v[52:53], v[16:17], v[0:1]
	v_pk_fma_f32 v[54:55], v[54:55], v[18:19], v[2:3]
	v_pk_mul_f32 v[26:27], v[26:27], v[38:39] op_sel_hi:[1,0]
	v_pk_mul_f32 v[52:53], v[54:55], v[38:39] op_sel_hi:[1,0]
	v_med3_f32 v26, v26, s9, v200
	v_med3_f32 v37, v27, s9, v200
	v_mov_b32_e32 v27, v169
	v_cvt_pk_fp8_f32 v27, v26, v37
	v_pk_fma_f32 v[48:49], v[48:49], v[22:23], v[4:5]
	v_med3_f32 v26, v52, s9, v200
	v_med3_f32 v37, v53, s9, v200
	v_pk_mul_f32 v[48:49], v[48:49], v[38:39] op_sel_hi:[1,0]
	v_cvt_pk_fp8_f32 v27, v26, v37 op_sel:[0,0,1]
	v_med3_f32 v37, v48, s9, v200
	v_med3_f32 v39, v49, s9, v200
	v_mov_b32_e32 v26, v169
	v_pk_fma_f32 v[50:51], v[50:51], v[20:21], v[6:7]
	v_cvt_pk_fp8_f32 v26, v37, v39
	v_pk_mul_f32 v[48:49], v[50:51], v[38:39] op_sel_hi:[1,0]
	v_pk_fma_f32 v[50:51], v[78:79], v[28:29], v[10:11]
	v_med3_f32 v37, v48, s9, v200
	v_med3_f32 v39, v49, s9, v200
	v_pk_fma_f32 v[48:49], v[76:77], v[30:31], v[8:9]
	v_cvt_pk_fp8_f32 v26, v37, v39 op_sel:[0,0,1]
	v_pk_mul_f32 v[48:49], v[48:49], v[38:39] op_sel_hi:[1,0]
	v_pk_fma_f32 v[52:53], v[72:73], v[34:35], v[12:13]
	v_med3_f32 v37, v48, s9, v200
	v_med3_f32 v39, v49, s9, v200
	v_mov_b32_e32 v49, v169
	v_cvt_pk_fp8_f32 v49, v37, v39
	v_pk_mul_f32 v[50:51], v[50:51], v[38:39] op_sel_hi:[1,0]
	v_mov_b32_e32 v48, v169
	v_med3_f32 v39, v51, s9, v200
	v_med3_f32 v37, v50, s9, v200
	v_pk_mul_f32 v[52:53], v[52:53], v[38:39] op_sel_hi:[1,0]
	v_cvt_pk_fp8_f32 v49, v37, v39 op_sel:[0,0,1]
	v_med3_f32 v37, v52, s9, v200
	v_med3_f32 v39, v53, s9, v200
	v_cvt_pk_fp8_f32 v48, v37, v39
	ds_read_b32 v39, v36 offset:2752
	v_pk_fma_f32 v[50:51], v[74:75], v[32:33], v[14:15]
	v_pk_fma_f32 v[12:13], v[68:69], v[34:35], v[12:13]
	v_pk_fma_f32 v[8:9], v[64:65], v[30:31], v[8:9]
	v_pk_fma_f32 v[4:5], v[44:45], v[22:23], v[4:5]
	s_waitcnt lgkmcnt(0)
	v_pk_mul_f32 v[36:37], v[50:51], v[38:39] op_sel_hi:[1,0]
	v_pk_fma_f32 v[0:1], v[40:41], v[16:17], v[0:1]
	v_med3_f32 v36, v36, s9, v200
	v_med3_f32 v37, v37, s9, v200
	v_cvt_pk_fp8_f32 v48, v36, v37 op_sel:[0,0,1]
	v_mul_f32_e32 v36, 0x41800000, v39
	v_pk_mul_f32 v[12:13], v[12:13], v[36:37] op_sel_hi:[1,0]
	v_pk_mul_f32 v[8:9], v[8:9], v[36:37] op_sel_hi:[1,0]
	v_pk_mul_f32 v[4:5], v[4:5], v[36:37] op_sel_hi:[1,0]
	v_pk_mul_f32 v[0:1], v[0:1], v[36:37] op_sel_hi:[1,0]
	v_pk_fma_f32 v[10:11], v[66:67], v[28:29], v[10:11]
	v_med3_f32 v12, v12, s9, v200
	v_med3_f32 v8, v8, s9, v200
	v_med3_f32 v13, v13, s9, v200
	v_med3_f32 v9, v9, s9, v200
	v_mov_b32_e32 v50, v169
	v_mov_b32_e32 v51, v169
	v_med3_f32 v4, v4, s9, v200
	v_med3_f32 v0, v0, s9, v200
	v_med3_f32 v5, v5, s9, v200
	v_med3_f32 v1, v1, s9, v200
	v_mov_b32_e32 v28, v169
	v_mov_b32_e32 v29, v169
	v_cvt_pk_fp8_f32 v50, v12, v13
	v_cvt_pk_fp8_f32 v51, v8, v9
	v_cvt_pk_fp8_f32 v28, v4, v5
	v_cvt_pk_fp8_f32 v29, v0, v1
	v_pk_fma_f32 v[14:15], v[70:71], v[32:33], v[14:15]
	v_pk_fma_f32 v[6:7], v[46:47], v[20:21], v[6:7]
	v_pk_fma_f32 v[2:3], v[42:43], v[18:19], v[2:3]
	v_pk_mul_f32 v[14:15], v[14:15], v[36:37] op_sel_hi:[1,0]
	v_pk_mul_f32 v[10:11], v[10:11], v[36:37] op_sel_hi:[1,0]
	v_pk_mul_f32 v[6:7], v[6:7], v[36:37] op_sel_hi:[1,0]
	v_pk_mul_f32 v[2:3], v[2:3], v[36:37] op_sel_hi:[1,0]
	v_med3_f32 v14, v14, s9, v200
	v_med3_f32 v10, v10, s9, v200
	v_med3_f32 v8, v15, s9, v200
	v_med3_f32 v9, v11, s9, v200
	v_med3_f32 v6, v6, s9, v200
	v_med3_f32 v2, v2, s9, v200
	v_med3_f32 v0, v7, s9, v200
	v_med3_f32 v1, v3, s9, v200
	v_cvt_pk_fp8_f32 v50, v14, v8 op_sel:[0,0,1]
	v_cvt_pk_fp8_f32 v51, v10, v9 op_sel:[0,0,1]
	v_cvt_pk_fp8_f32 v28, v6, v0 op_sel:[0,0,1]
	v_cvt_pk_fp8_f32 v29, v2, v1 op_sel:[0,0,1]
	v_cndmask_b32_e32 v0, v25, v24, vcc
	v_ashrrev_i32_e32 v1, 31, v0
	v_lshlrev_b64 v[0:1], 10, v[0:1]
	v_lshl_add_u64 v[0:1], s[30:31], 0, v[0:1]
	v_lshl_add_u64 v[0:1], v[0:1], 0, v[168:169]
	v_permlane16_swap_b32_e32 v48, v50
	v_permlane16_swap_b32_e32 v49, v51
	v_permlane16_swap_b32_e32 v26, v28
	v_permlane16_swap_b32_e32 v27, v29
	s_cmp_eq_u32 s74, s67
	s_mov_b64 s[36:37], -1
	global_store_dwordx4 v[0:1], v[48:51], off
	global_store_dwordx4 v[0:1], v[26:29], off offset:128
	s_cbranch_scc1 .LBB0_944
	s_andn2_b64 vcc, exec, s[14:15]
	s_cbranch_vccnz .LBB0_943
	s_barrier
	s_branch .LBB0_943
